# conversion stores without nt (write-back L2 ack)
# baseline (speedup 1.0000x reference)
; __device__ __forceinline__ unsigned cvt_pk_bf16(float lo, float hi) { unsigned r; asm volatile("v_cvt_pk_bf16_f32 %0, %1, %2" : "=v"(r) : "v"(lo), "v"(hi)); return r; }
; #define GAS __attribute__((address_space(1)))
; #define LAS __attribute__((address_space(3)))
; __device__ __forceinline__ void conv_load(const ConvSrc& c, int lane, f32x4 (&ra)[8], f32x4 (&rb)[8]) {
;     const int nblk = c.N >> 6, kb = c.kfast ? (c.item & 31) : c.item / nblk, nb = c.kfast ? (c.item >> 5) : c.item - kb * nblk, k0 = kb * 64, n0 = nb * 64;
;     const int n4 = (lane & 15) * 4, kq = lane >> 4;
; #pragma unroll
;     for (int i = 0; i < 8; ++i) { const int kp2 = 4 * i + kq; const float* p = c.W + (size_t)(k0 + 2 * kp2) * c.N + n0 + n4; ra[i] = __builtin_nontemporal_load((const GAS f32x4*)p); rb[i] = __builtin_nontemporal_load((const GAS f32x4*)(p + c.N)); }
; }
; __device__ __forceinline__ void conv_emit(const ConvSrc& c, int lane, LAS unsigned* P, const f32x4 (&ra)[8], const f32x4 (&rb)[8]) {
;     const int nblk = c.N >> 6, kb = c.kfast ? (c.item & 31) : c.item / nblk, nb = c.kfast ? (c.item >> 5) : c.item - kb * nblk, k0 = kb * 64, n0 = nb * 64;
;     const int n4 = (lane & 15) * 4, kq = lane >> 4;
; #pragma unroll
;     for (int i = 0; i < 8; ++i) { const int kp2 = 4 * i + kq; LAS unsigned* d = P + kp2 * 65 + n4;
;         d[0] = pg8::cvt_pk_bf16(ra[i].x, rb[i].x); d[1] = pg8::cvt_pk_bf16(ra[i].y, rb[i].y); d[2] = pg8::cvt_pk_bf16(ra[i].z, rb[i].z); d[3] = pg8::cvt_pk_bf16(ra[i].w, rb[i].w); }
.LBB0_30:
	s_lshr_b32 s4, s2, 6
	v_cvt_f32_u32_e32 v0, s4
	s_sub_i32 s34, 0, s4
	s_abs_i32 s29, s17
	s_ashr_i32 s21, s17, 31
	v_rcp_iflag_f32_e32 v0, v0
	v_mov_b32_e32 v131, v129
	v_mul_f32_e32 v0, 0x4f7ffffe, v0
	v_cvt_u32_f32_e32 v0, v0
	s_nop 0
	v_readfirstlane_b32 s35, v0
	s_mul_i32 s34, s34, s35
	s_mul_hi_u32 s34, s35, s34
	s_add_i32 s35, s35, s34
	s_mul_hi_u32 s34, s29, s35
	s_mul_i32 s35, s34, s4
	s_sub_i32 s29, s29, s35
	s_add_i32 s36, s34, 1
	s_sub_i32 s35, s29, s4
	s_cmp_ge_u32 s29, s4
	s_cselect_b32 s34, s36, s34
	s_cselect_b32 s29, s35, s29
	s_add_i32 s35, s34, 1
	s_cmp_ge_u32 s29, s4
	s_cselect_b32 s29, s35, s34
	s_xor_b32 s29, s29, s21
	s_sub_i32 s21, s29, s21
	v_lshl_add_u32 v28, s21, 6, v133
	s_mul_i32 s4, s21, s4
	v_mad_u64_u32 v[0:1], s[34:35], v28, s2, 0
	s_sub_i32 s4, s17, s4
	v_ashrrev_i32_e32 v3, 31, v28
	v_mov_b32_e32 v2, v1
	s_lshl_b32 s34, s4, 6
	v_mad_u64_u32 v[2:3], s[36:37], v3, s2, v[2:3]
	s_ashr_i32 s35, s34, 31
	v_mov_b32_e32 v1, v2
	s_waitcnt lgkmcnt(0)
	v_lshl_add_u64 v[0:1], v[0:1], 2, s[30:31]
	s_lshl_b64 s[34:35], s[34:35], 2
	v_lshl_add_u64 v[0:1], v[0:1], 0, s[34:35]
	v_lshl_add_u64 v[0:1], v[0:1], 0, v[128:129]
	s_lshl_b64 s[36:37], s[2:3], 2
	v_lshl_add_u64 v[4:5], v[0:1], 0, s[36:37]
	global_load_dwordx4 v[0:3], v[0:1], off nt
	s_nop 0
	global_load_dwordx4 v[32:35], v[4:5], off nt
	v_add_u32_e32 v4, 8, v28
	v_ashrrev_i32_e32 v7, 31, v4
	v_mad_u64_u32 v[4:5], s[44:45], v4, s2, 0
	v_mov_b32_e32 v6, v5
	v_mad_u64_u32 v[6:7], s[44:45], v7, s2, v[6:7]
	v_mov_b32_e32 v5, v6
	v_lshl_add_u64 v[4:5], v[4:5], 2, s[30:31]
	v_lshl_add_u64 v[4:5], v[4:5], 0, s[34:35]
	v_lshl_add_u64 v[4:5], v[4:5], 0, v[128:129]
	v_lshl_add_u64 v[8:9], v[4:5], 0, s[36:37]
	global_load_dwordx4 v[4:7], v[4:5], off nt
	s_nop 0
	global_load_dwordx4 v[44:47], v[8:9], off nt
	v_add_u32_e32 v8, 16, v28
	v_ashrrev_i32_e32 v11, 31, v8
	v_mad_u64_u32 v[8:9], s[44:45], v8, s2, 0
	v_mov_b32_e32 v10, v9
	v_mad_u64_u32 v[10:11], s[44:45], v11, s2, v[10:11]
	v_mov_b32_e32 v9, v10
	v_lshl_add_u64 v[8:9], v[8:9], 2, s[30:31]
	v_lshl_add_u64 v[8:9], v[8:9], 0, s[34:35]
	v_lshl_add_u64 v[8:9], v[8:9], 0, v[128:129]
	v_lshl_add_u64 v[12:13], v[8:9], 0, s[36:37]
	global_load_dwordx4 v[8:11], v[8:9], off nt
	s_nop 0
	global_load_dwordx4 v[48:51], v[12:13], off nt
	v_add_u32_e32 v12, 24, v28
	v_ashrrev_i32_e32 v15, 31, v12
	v_mad_u64_u32 v[12:13], s[44:45], v12, s2, 0
	v_mov_b32_e32 v14, v13
	v_mad_u64_u32 v[14:15], s[44:45], v15, s2, v[14:15]
	v_mov_b32_e32 v13, v14
	v_lshl_add_u64 v[12:13], v[12:13], 2, s[30:31]
	v_lshl_add_u64 v[12:13], v[12:13], 0, s[34:35]
	v_lshl_add_u64 v[12:13], v[12:13], 0, v[128:129]
	v_lshl_add_u64 v[16:17], v[12:13], 0, s[36:37]
	global_load_dwordx4 v[12:15], v[12:13], off nt
	s_nop 0
	global_load_dwordx4 v[52:55], v[16:17], off nt
	v_add_u32_e32 v16, 32, v28
	v_ashrrev_i32_e32 v19, 31, v16
	v_mad_u64_u32 v[16:17], s[44:45], v16, s2, 0
	v_mov_b32_e32 v18, v17
	v_mad_u64_u32 v[18:19], s[44:45], v19, s2, v[18:19]
	v_mov_b32_e32 v17, v18
	v_lshl_add_u64 v[16:17], v[16:17], 2, s[30:31]
	v_lshl_add_u64 v[16:17], v[16:17], 0, s[34:35]
	v_lshl_add_u64 v[16:17], v[16:17], 0, v[128:129]
	v_lshl_add_u64 v[20:21], v[16:17], 0, s[36:37]
	global_load_dwordx4 v[16:19], v[16:17], off nt
	s_nop 0
	global_load_dwordx4 v[56:59], v[20:21], off nt
	v_add_u32_e32 v20, 40, v28
	v_ashrrev_i32_e32 v23, 31, v20
	v_mad_u64_u32 v[20:21], s[44:45], v20, s2, 0
	v_mov_b32_e32 v22, v21
	v_mad_u64_u32 v[22:23], s[44:45], v23, s2, v[22:23]
	v_mov_b32_e32 v21, v22
	v_lshl_add_u64 v[20:21], v[20:21], 2, s[30:31]
	v_lshl_add_u64 v[20:21], v[20:21], 0, s[34:35]
	v_lshl_add_u64 v[20:21], v[20:21], 0, v[128:129]
	v_lshl_add_u64 v[24:25], v[20:21], 0, s[36:37]
	global_load_dwordx4 v[20:23], v[20:21], off nt
	s_nop 0
	global_load_dwordx4 v[60:63], v[24:25], off nt
	v_add_u32_e32 v24, 48, v28
	v_ashrrev_i32_e32 v27, 31, v24
	v_mad_u64_u32 v[24:25], s[44:45], v24, s2, 0
	v_mov_b32_e32 v26, v25
	v_mad_u64_u32 v[26:27], s[44:45], v27, s2, v[26:27]
	v_mov_b32_e32 v25, v26
	v_lshl_add_u64 v[24:25], v[24:25], 2, s[30:31]
	v_lshl_add_u64 v[24:25], v[24:25], 0, s[34:35]
	v_lshl_add_u64 v[24:25], v[24:25], 0, v[128:129]
	v_lshl_add_u64 v[26:27], v[24:25], 0, s[36:37]
	global_load_dwordx4 v[36:39], v[24:25], off nt
	global_load_dwordx4 v[40:43], v[26:27], off nt
	v_add_u32_e32 v24, 56, v28
	v_ashrrev_i32_e32 v27, 31, v24
	v_mad_u64_u32 v[24:25], s[44:45], v24, s2, 0
	v_mov_b32_e32 v26, v25
	v_mad_u64_u32 v[26:27], s[44:45], v27, s2, v[26:27]
	v_mov_b32_e32 v25, v26
	v_lshl_add_u64 v[24:25], v[24:25], 2, s[30:31]
	v_lshl_add_u64 v[24:25], v[24:25], 0, s[34:35]
	v_lshl_add_u64 v[24:25], v[24:25], 0, v[128:129]
	v_lshl_add_u64 v[26:27], v[24:25], 0, s[36:37]
	global_load_dwordx4 v[28:31], v[24:25], off nt
	s_nop 0
	global_load_dwordx4 v[24:27], v[26:27], off nt
	s_waitcnt vmcnt(38)
	v_cvt_pk_bf16_f32 v120, v120, v124
	ds_write_b32 v140, v120
	v_cvt_pk_bf16_f32 v120, v121, v125
	ds_write_b32 v140, v120 offset:4
	v_cvt_pk_bf16_f32 v120, v122, v126
	ds_write_b32 v140, v120 offset:8
	v_cvt_pk_bf16_f32 v120, v123, v127
	ds_write_b32 v140, v120 offset:12
	s_waitcnt vmcnt(36)
	v_cvt_pk_bf16_f32 v112, v112, v116
	ds_write_b32 v140, v112 offset:1040
	v_cvt_pk_bf16_f32 v112, v113, v117
	ds_write_b32 v140, v112 offset:1044
	v_cvt_pk_bf16_f32 v112, v114, v118
	ds_write_b32 v140, v112 offset:1048
	v_cvt_pk_bf16_f32 v112, v115, v119
	ds_write_b32 v140, v112 offset:1052
	s_waitcnt vmcnt(34)
; #define GAS __attribute__((address_space(1)))
; #define LAS __attribute__((address_space(3)))
; #define LDS_WAIT() asm volatile("s_waitcnt lgkmcnt(0)" ::: "memory")
; __device__ __forceinline__ void conv_emit(const ConvSrc& c, int lane, LAS unsigned* P, const f32x4 (&ra)[8], const f32x4 (&rb)[8]) {
;     ...
;     LDS_WAIT(); asm volatile("" ::: "memory");
;     const int cc = lane & 7;
; #pragma unroll
;     for (int jj = 0; jj < 8; ++jj) { const int n = (lane >> 3) + 8 * jj; const LAS unsigned* sp = P + (4 * cc) * 65 + n;
;         v4u o; o.x = sp[0]; o.y = sp[65]; o.z = sp[130]; o.w = sp[195];
;         bf16* dst = c.tiled ? c.WT + (size_t)((nb >> 2) * c.tiled + c.ktoff + kb) * 16384 + ((nb & 3) * 64 + n) * 64 + 8 * cc : c.WT + (size_t)(n0 + n) * c.ldk + k0 + 8 * cc;
;         __builtin_nontemporal_store(o, (GAS v4u*)dst); }
;     LDS_WAIT(); asm volatile("" ::: "memory");
	v_cvt_pk_bf16_f32 v104, v104, v108
	ds_write_b32 v140, v104 offset:2080
	v_cvt_pk_bf16_f32 v104, v105, v109
	ds_write_b32 v140, v104 offset:2084
	v_cvt_pk_bf16_f32 v104, v106, v110
	ds_write_b32 v140, v104 offset:2088
	v_cvt_pk_bf16_f32 v104, v107, v111
	ds_write_b32 v140, v104 offset:2092
	s_waitcnt vmcnt(32)
	v_cvt_pk_bf16_f32 v96, v96, v100
	ds_write_b32 v140, v96 offset:3120
	v_cvt_pk_bf16_f32 v96, v97, v101
	ds_write_b32 v140, v96 offset:3124
	v_cvt_pk_bf16_f32 v96, v98, v102
	ds_write_b32 v140, v96 offset:3128
	v_cvt_pk_bf16_f32 v96, v99, v103
	ds_write_b32 v140, v96 offset:3132
	s_waitcnt vmcnt(30)
	v_cvt_pk_bf16_f32 v88, v88, v92
	ds_write_b32 v140, v88 offset:4160
	v_cvt_pk_bf16_f32 v88, v89, v93
	ds_write_b32 v140, v88 offset:4164
	v_cvt_pk_bf16_f32 v88, v90, v94
	ds_write_b32 v140, v88 offset:4168
	v_cvt_pk_bf16_f32 v88, v91, v95
	ds_write_b32 v140, v88 offset:4172
	s_waitcnt vmcnt(28)
	v_cvt_pk_bf16_f32 v80, v80, v84
	ds_write_b32 v140, v80 offset:5200
	v_cvt_pk_bf16_f32 v80, v81, v85
	ds_write_b32 v140, v80 offset:5204
	v_cvt_pk_bf16_f32 v80, v82, v86
	ds_write_b32 v140, v80 offset:5208
	v_cvt_pk_bf16_f32 v80, v83, v87
	ds_write_b32 v140, v80 offset:5212
	s_waitcnt vmcnt(26)
	v_cvt_pk_bf16_f32 v72, v72, v76
	ds_write_b32 v140, v72 offset:6240
	v_cvt_pk_bf16_f32 v72, v73, v77
	ds_write_b32 v140, v72 offset:6244
	v_cvt_pk_bf16_f32 v72, v74, v78
	ds_write_b32 v140, v72 offset:6248
	v_cvt_pk_bf16_f32 v72, v75, v79
	ds_write_b32 v140, v72 offset:6252
	s_waitcnt vmcnt(24)
	v_cvt_pk_bf16_f32 v64, v64, v68
	ds_write_b32 v140, v64 offset:7280
	v_cvt_pk_bf16_f32 v64, v65, v69
	ds_write_b32 v140, v64 offset:7284
	v_cvt_pk_bf16_f32 v64, v66, v70
	ds_write_b32 v140, v64 offset:7288
	v_cvt_pk_bf16_f32 v64, v67, v71
	ds_write_b32 v140, v64 offset:7292
	s_ashr_i32 s4, s43, 2
	s_waitcnt lgkmcnt(0)
	s_mul_i32 s4, s4, s42
	s_add_i32 s5, s20, s5
	s_add_i32 s4, s5, s4
	ds_read2_b32 v[72:73], v134 offset1:8
	ds_read2_b32 v[64:65], v134 offset0:65 offset1:73
	ds_read2_b32 v[74:75], v134 offset0:130 offset1:138
	ds_read2_b32 v[66:67], v134 offset0:195 offset1:203
	s_ashr_i32 s5, s4, 31
	s_and_b32 s21, s28, 0xc0
	s_lshl_b64 s[4:5], s[4:5], 15
	s_add_u32 s26, s26, s4
	v_add_lshl_u32 v76, s21, v132, 6
	s_addc_u32 s27, s27, s5
	v_ashrrev_i32_e32 v77, 31, v76
	v_lshl_add_u64 v[76:77], v[76:77], 1, s[26:27]
	s_waitcnt lgkmcnt(3)
	v_mov_b32_e32 v68, v72
	s_waitcnt lgkmcnt(2)
	v_mov_b32_e32 v69, v64
	s_waitcnt lgkmcnt(1)
	v_mov_b32_e32 v70, v74
	s_waitcnt lgkmcnt(0)
	v_mov_b32_e32 v71, v66
	v_lshl_add_u64 v[76:77], v[76:77], 0, v[130:131]
	global_store_dwordx4 v[76:77], v[68:71], off
	v_mov_b32_e32 v64, v73
	v_mov_b32_e32 v66, v75
	v_add_lshl_u32 v68, s21, v135, 6
	v_ashrrev_i32_e32 v69, 31, v68
	v_lshl_add_u64 v[68:69], v[68:69], 1, s[26:27]
	v_lshl_add_u64 v[72:73], v[68:69], 0, v[130:131]
	ds_read2_b32 v[74:75], v134 offset0:16 offset1:24
	ds_read2_b32 v[68:69], v134 offset0:81 offset1:89
	ds_read2_b32 v[76:77], v134 offset0:146 offset1:154
	ds_read2_b32 v[70:71], v134 offset0:211 offset1:219
	global_store_dwordx4 v[72:73], v[64:67], off
	v_add_lshl_u32 v72, s21, v136, 6
	v_ashrrev_i32_e32 v73, 31, v72
	v_lshl_add_u64 v[72:73], v[72:73], 1, s[26:27]
	s_waitcnt lgkmcnt(3)
	v_mov_b32_e32 v64, v74
	s_waitcnt lgkmcnt(2)
	v_mov_b32_e32 v65, v68
	s_waitcnt lgkmcnt(1)
	v_mov_b32_e32 v66, v76
	s_waitcnt lgkmcnt(0)
	v_mov_b32_e32 v67, v70
	v_lshl_add_u64 v[72:73], v[72:73], 0, v[130:131]
	global_store_dwordx4 v[72:73], v[64:67], off
	v_mov_b32_e32 v68, v75
	v_mov_b32_e32 v70, v77
	v_add_lshl_u32 v64, s21, v137, 6
	v_ashrrev_i32_e32 v65, 31, v64
	v_lshl_add_u64 v[64:65], v[64:65], 1, s[26:27]
	v_lshl_add_u64 v[72:73], v[64:65], 0, v[130:131]
	ds_read2_b32 v[74:75], v134 offset0:32 offset1:40
	ds_read2_b32 v[64:65], v134 offset0:97 offset1:105
	ds_read2_b32 v[76:77], v134 offset0:162 offset1:170
	ds_read2_b32 v[66:67], v134 offset0:227 offset1:235
	global_store_dwordx4 v[72:73], v[68:71], off
	v_add_lshl_u32 v72, s21, v138, 6
	v_ashrrev_i32_e32 v73, 31, v72
	v_lshl_add_u64 v[72:73], v[72:73], 1, s[26:27]
	s_waitcnt lgkmcnt(3)
	v_mov_b32_e32 v68, v74
	s_waitcnt lgkmcnt(2)
	v_mov_b32_e32 v69, v64
	s_waitcnt lgkmcnt(1)
	v_mov_b32_e32 v70, v76
	s_waitcnt lgkmcnt(0)
	v_mov_b32_e32 v71, v66
	v_lshl_add_u64 v[72:73], v[72:73], 0, v[130:131]
	global_store_dwordx4 v[72:73], v[68:71], off
	v_mov_b32_e32 v64, v75
	v_mov_b32_e32 v66, v77
	v_add_lshl_u32 v68, s21, v139, 6
	v_ashrrev_i32_e32 v69, 31, v68
	v_lshl_add_u64 v[68:69], v[68:69], 1, s[26:27]
	v_lshl_add_u64 v[72:73], v[68:69], 0, v[130:131]
	ds_read2_b32 v[74:75], v134 offset0:48 offset1:56
	ds_read2_b32 v[68:69], v134 offset0:113 offset1:121
	ds_read2_b32 v[76:77], v134 offset0:178 offset1:186
	ds_read2_b32 v[70:71], v134 offset0:243 offset1:251
	global_store_dwordx4 v[72:73], v[64:67], off
	v_add_lshl_u32 v72, s21, v141, 6
	v_ashrrev_i32_e32 v73, 31, v72
	v_lshl_add_u64 v[72:73], v[72:73], 1, s[26:27]
	s_waitcnt lgkmcnt(3)
	v_mov_b32_e32 v64, v74
	s_waitcnt lgkmcnt(2)
	v_mov_b32_e32 v65, v68
	s_waitcnt lgkmcnt(1)
	v_mov_b32_e32 v66, v76
	s_waitcnt lgkmcnt(0)
	v_mov_b32_e32 v67, v70
	v_lshl_add_u64 v[72:73], v[72:73], 0, v[130:131]
	global_store_dwordx4 v[72:73], v[64:67], off
	v_mov_b32_e32 v68, v75
	v_mov_b32_e32 v70, v77
	v_add_lshl_u32 v64, s21, v142, 6
	v_ashrrev_i32_e32 v65, 31, v64
	v_lshl_add_u64 v[64:65], v[64:65], 1, s[26:27]
	v_lshl_add_u64 v[64:65], v[64:65], 0, v[130:131]
	global_store_dwordx4 v[64:65], v[68:71], off
	s_waitcnt lgkmcnt(0)
	s_cmpk_gt_i32 s22, 0x2bff
	s_mov_b32 s21, s2
	s_cbranch_scc1 .LBB0_71

; #define GAS __attribute__((address_space(1)))
; __device__ __forceinline__ void conv_load(const ConvSrc& c, int lane, f32x4 (&ra)[8], f32x4 (&rb)[8]) {
;     const int nblk = c.N >> 6, kb = c.kfast ? (c.item & 31) : c.item / nblk, nb = c.kfast ? (c.item >> 5) : c.item - kb * nblk, k0 = kb * 64, n0 = nb * 64;
;     const int n4 = (lane & 15) * 4, kq = lane >> 4;
; #pragma unroll
;     for (int i = 0; i < 8; ++i) { const int kp2 = 4 * i + kq; const float* p = c.W + (size_t)(k0 + 2 * kp2) * c.N + n0 + n4; ra[i] = __builtin_nontemporal_load((const GAS f32x4*)p); rb[i] = __builtin_nontemporal_load((const GAS f32x4*)(p + c.N)); }
; }
.LBB0_50:
	s_lshr_b32 s34, s2, 6
	v_cvt_f32_u32_e32 v64, s34
	s_sub_i32 s29, 0, s34
	s_abs_i32 s28, s4
	s_ashr_i32 s20, s4, 31
	v_rcp_iflag_f32_e32 v64, v64
	v_mov_b32_e32 v131, v129
	v_mul_f32_e32 v64, 0x4f7ffffe, v64
	v_cvt_u32_f32_e32 v64, v64
	s_nop 0
	v_readfirstlane_b32 s35, v64
	s_mul_i32 s29, s29, s35
	s_mul_hi_u32 s29, s35, s29
	s_add_i32 s35, s35, s29
	s_mul_hi_u32 s29, s28, s35
	s_mul_i32 s35, s29, s34
	s_sub_i32 s28, s28, s35
	s_add_i32 s36, s29, 1
	s_sub_i32 s35, s28, s34
	s_cmp_ge_u32 s28, s34
	s_cselect_b32 s29, s36, s29
	s_cselect_b32 s28, s35, s28
	s_add_i32 s35, s29, 1
	s_cmp_ge_u32 s28, s34
	s_cselect_b32 s28, s35, s29
	s_xor_b32 s28, s28, s20
	s_sub_i32 s20, s28, s20
	v_lshl_add_u32 v80, s20, 6, v133
	v_mad_u64_u32 v[64:65], s[28:29], v80, s2, 0
	v_ashrrev_i32_e32 v67, 31, v80
	v_mov_b32_e32 v66, v65
	v_add_u32_e32 v68, 8, v80
	v_mad_u64_u32 v[66:67], s[28:29], v67, s2, v[66:67]
	v_mov_b32_e32 v65, v66
	v_mad_u64_u32 v[66:67], s[28:29], v68, s2, 0
	v_ashrrev_i32_e32 v69, 31, v68
	v_mov_b32_e32 v68, v67
	v_mad_u64_u32 v[68:69], s[28:29], v69, s2, v[68:69]
	v_mov_b32_e32 v67, v68
	v_add_u32_e32 v68, 16, v80
	v_ashrrev_i32_e32 v71, 31, v68
	v_mad_u64_u32 v[68:69], s[28:29], v68, s2, 0
	v_mov_b32_e32 v70, v69
	v_mad_u64_u32 v[70:71], s[28:29], v71, s2, v[70:71]
	v_mov_b32_e32 v69, v70
	v_add_u32_e32 v70, 24, v80
	v_ashrrev_i32_e32 v73, 31, v70
	v_mad_u64_u32 v[70:71], s[28:29], v70, s2, 0
	v_mov_b32_e32 v72, v71
	v_mad_u64_u32 v[72:73], s[28:29], v73, s2, v[72:73]
	v_mov_b32_e32 v71, v72
	v_add_u32_e32 v72, 32, v80
	v_ashrrev_i32_e32 v75, 31, v72
	v_mad_u64_u32 v[72:73], s[28:29], v72, s2, 0
	v_mov_b32_e32 v74, v73
	v_mad_u64_u32 v[74:75], s[28:29], v75, s2, v[74:75]
	v_mov_b32_e32 v73, v74
	v_add_u32_e32 v74, 40, v80
	v_ashrrev_i32_e32 v77, 31, v74
	v_mad_u64_u32 v[74:75], s[28:29], v74, s2, 0
	v_mov_b32_e32 v76, v75
	v_mad_u64_u32 v[76:77], s[28:29], v77, s2, v[76:77]
	v_mov_b32_e32 v75, v76
	v_add_u32_e32 v76, 48, v80
	v_ashrrev_i32_e32 v79, 31, v76
	v_mad_u64_u32 v[76:77], s[28:29], v76, s2, 0
	v_mov_b32_e32 v78, v77
	v_mad_u64_u32 v[78:79], s[28:29], v79, s2, v[78:79]
	v_mov_b32_e32 v77, v78
	v_add_u32_e32 v78, 56, v80
	v_ashrrev_i32_e32 v81, 31, v78
	v_mad_u64_u32 v[78:79], s[28:29], v78, s2, 0
	v_mov_b32_e32 v80, v79
	v_mad_u64_u32 v[80:81], s[28:29], v81, s2, v[80:81]
	s_mul_i32 s28, s20, s34
	s_sub_i32 s43, s4, s28
	s_lshl_b32 s28, s43, 6
	s_ashr_i32 s29, s28, 31
	v_mov_b32_e32 v79, v80
	s_waitcnt lgkmcnt(0)
	v_lshl_add_u64 v[64:65], v[64:65], 2, s[30:31]
	s_lshl_b64 s[34:35], s[28:29], 2
	v_lshl_add_u64 v[66:67], v[66:67], 2, s[30:31]
	v_lshl_add_u64 v[64:65], v[64:65], 0, s[34:35]
	v_lshl_add_u64 v[66:67], v[66:67], 0, s[34:35]
	v_lshl_add_u64 v[68:69], v[68:69], 2, s[30:31]
	v_lshl_add_u64 v[78:79], v[78:79], 2, s[30:31]
	v_lshl_add_u64 v[64:65], v[64:65], 0, v[128:129]
	s_lshl_b64 s[36:37], s[2:3], 2
	v_lshl_add_u64 v[66:67], v[66:67], 0, v[128:129]
	v_lshl_add_u64 v[68:69], v[68:69], 0, s[34:35]
	v_lshl_add_u64 v[70:71], v[70:71], 2, s[30:31]
	v_lshl_add_u64 v[78:79], v[78:79], 0, s[34:35]
	v_lshl_add_u64 v[68:69], v[68:69], 0, v[128:129]
	v_lshl_add_u64 v[70:71], v[70:71], 0, s[34:35]
	v_lshl_add_u64 v[72:73], v[72:73], 2, s[30:31]
	v_lshl_add_u64 v[144:145], v[78:79], 0, v[128:129]
	v_lshl_add_u64 v[78:79], v[64:65], 0, s[36:37]
	global_load_dwordx4 v[120:123], v[64:65], off nt
	global_load_dwordx4 v[124:127], v[78:79], off nt
	v_lshl_add_u64 v[64:65], v[66:67], 0, s[36:37]
	v_lshl_add_u64 v[70:71], v[70:71], 0, v[128:129]
	v_lshl_add_u64 v[72:73], v[72:73], 0, s[34:35]
	v_lshl_add_u64 v[74:75], v[74:75], 2, s[30:31]
	global_load_dwordx4 v[112:115], v[66:67], off nt
	global_load_dwordx4 v[116:119], v[64:65], off nt
	v_lshl_add_u64 v[64:65], v[68:69], 0, s[36:37]
	v_lshl_add_u64 v[72:73], v[72:73], 0, v[128:129]
	v_lshl_add_u64 v[74:75], v[74:75], 0, s[34:35]
	v_lshl_add_u64 v[76:77], v[76:77], 2, s[30:31]
	global_load_dwordx4 v[104:107], v[68:69], off nt
	global_load_dwordx4 v[108:111], v[64:65], off nt
	v_lshl_add_u64 v[64:65], v[70:71], 0, s[36:37]
	v_lshl_add_u64 v[74:75], v[74:75], 0, v[128:129]
	v_lshl_add_u64 v[76:77], v[76:77], 0, s[34:35]
	global_load_dwordx4 v[96:99], v[70:71], off nt
	global_load_dwordx4 v[100:103], v[64:65], off nt
	v_lshl_add_u64 v[64:65], v[72:73], 0, s[36:37]
	v_lshl_add_u64 v[76:77], v[76:77], 0, v[128:129]
	global_load_dwordx4 v[88:91], v[72:73], off nt
	global_load_dwordx4 v[92:95], v[64:65], off nt
	v_lshl_add_u64 v[64:65], v[74:75], 0, s[36:37]
	global_load_dwordx4 v[80:83], v[74:75], off nt
	global_load_dwordx4 v[84:87], v[64:65], off nt
	v_lshl_add_u64 v[64:65], v[76:77], 0, s[36:37]
	v_lshl_add_u64 v[68:69], v[144:145], 0, s[36:37]
	global_load_dwordx4 v[72:75], v[76:77], off nt
	s_nop 0
	global_load_dwordx4 v[76:79], v[64:65], off nt
	s_nop 0
	global_load_dwordx4 v[64:67], v[144:145], off nt
	s_nop 0
	global_load_dwordx4 v[68:71], v[68:69], off nt
	s_waitcnt vmcnt(16)
; #define GAS __attribute__((address_space(1)))
; #define LAS __attribute__((address_space(3)))
; __device__ __forceinline__ ConvSrc conv_decode(KP kp, unsigned char* ws, int it) {
;     constexpr int I_IN = 32 * 256, I_SQ = 32 * 32, I_UP = 32 * 64, I_DN = 32 * 32;
;     ConvSrc c; int r = it; c.ldk = 2048; c.kfast = 0; c.tiled = 32; c.ktoff = 0;
;     if (r < I_IN) { c.W = (const float*)KIN(6); c.WT = (bf16*)(ws + WS_WIN); c.N = 16384; c.item = r; return c; } r -= I_IN;
;     if (r < I_SQ) { c.W = (const float*)KIN(13); c.WT = (bf16*)(ws + WS_WAO); c.N = 2048; c.item = r; c.ldk = 4096; c.tiled = 64; return c; } r -= I_SQ;
;     if (r < I_SQ) { c.W = (const float*)KIN(14); c.WT = (bf16*)(ws + WS_WAO); c.N = 2048; c.item = r; c.ldk = 4096; c.tiled = 64; c.ktoff = 32; return c; } r -= I_SQ;
;     if (r < I_SQ) { c.W = (const float*)KIN(15); c.WT = (bf16*)(ws + WS_WO); c.N = 2048; c.item = r; return c; } r -= I_SQ;
;     if (r < NE * I_UP) { const int e = r / I_UP; c.W = (const float*)KIN(19) + (size_t)e * 2048 * 4096; c.WT = (bf16*)(ws + WS_WUP) + (size_t)e * 4096 * 2048; c.N = 4096; c.item = r - e * I_UP; return c; } r -= NE * I_UP;
; __device__ __forceinline__ void conv_emit(const ConvSrc& c, int lane, LAS unsigned* P, const f32x4 (&ra)[8], const f32x4 (&rb)[8]) {
;     const int nblk = c.N >> 6, kb = c.kfast ? (c.item & 31) : c.item / nblk, nb = c.kfast ? (c.item >> 5) : c.item - kb * nblk, k0 = kb * 64, n0 = nb * 64;
;     const int n4 = (lane & 15) * 4, kq = lane >> 4;
; #pragma unroll
;     for (int i = 0; i < 8; ++i) { const int kp2 = 4 * i + kq; LAS unsigned* d = P + kp2 * 65 + n4;
;         d[0] = pg8::cvt_pk_bf16(ra[i].x, rb[i].x); d[1] = pg8::cvt_pk_bf16(ra[i].y, rb[i].y); d[2] = pg8::cvt_pk_bf16(ra[i].z, rb[i].z); d[3] = pg8::cvt_pk_bf16(ra[i].w, rb[i].w); }
;     LDS_WAIT(); asm volatile("" ::: "memory");
;     const int cc = lane & 7;
; #pragma unroll
;     for (int jj = 0; jj < 8; ++jj) { const int n = (lane >> 3) + 8 * jj; const LAS unsigned* sp = P + (4 * cc) * 65 + n;
;         v4u o; o.x = sp[0]; o.y = sp[65]; o.z = sp[130]; o.w = sp[195];
;         bf16* dst = c.tiled ? c.WT + (size_t)((nb >> 2) * c.tiled + c.ktoff + kb) * 16384 + ((nb & 3) * 64 + n) * 64 + 8 * cc : c.WT + (size_t)(n0 + n) * c.ldk + k0 + 8 * cc;
;         __builtin_nontemporal_store(o, (GAS v4u*)dst); }
;     LDS_WAIT(); asm volatile("" ::: "memory");
	v_cvt_pk_bf16_f32 v0, v0, v32
	ds_write_b32 v140, v0
	v_cvt_pk_bf16_f32 v0, v1, v33
	ds_write_b32 v140, v0 offset:4
	v_cvt_pk_bf16_f32 v0, v2, v34
	ds_write_b32 v140, v0 offset:8
	v_cvt_pk_bf16_f32 v0, v3, v35
	ds_write_b32 v140, v0 offset:12
	v_cvt_pk_bf16_f32 v0, v4, v44
	ds_write_b32 v140, v0 offset:1040
	v_cvt_pk_bf16_f32 v0, v5, v45
	ds_write_b32 v140, v0 offset:1044
	v_cvt_pk_bf16_f32 v0, v6, v46
	ds_write_b32 v140, v0 offset:1048
	v_cvt_pk_bf16_f32 v0, v7, v47
	ds_write_b32 v140, v0 offset:1052
	v_cvt_pk_bf16_f32 v0, v8, v48
	ds_write_b32 v140, v0 offset:2080
	v_cvt_pk_bf16_f32 v0, v9, v49
	ds_write_b32 v140, v0 offset:2084
	v_cvt_pk_bf16_f32 v0, v10, v50
	ds_write_b32 v140, v0 offset:2088
	v_cvt_pk_bf16_f32 v0, v11, v51
	ds_write_b32 v140, v0 offset:2092
	v_cvt_pk_bf16_f32 v0, v12, v52
	ds_write_b32 v140, v0 offset:3120
	v_cvt_pk_bf16_f32 v0, v13, v53
	ds_write_b32 v140, v0 offset:3124
	v_cvt_pk_bf16_f32 v0, v14, v54
	ds_write_b32 v140, v0 offset:3128
	v_cvt_pk_bf16_f32 v0, v15, v55
	ds_write_b32 v140, v0 offset:3132
	v_cvt_pk_bf16_f32 v0, v16, v56
	ds_write_b32 v140, v0 offset:4160
	v_cvt_pk_bf16_f32 v0, v17, v57
	ds_write_b32 v140, v0 offset:4164
	v_cvt_pk_bf16_f32 v0, v18, v58
	ds_write_b32 v140, v0 offset:4168
	v_cvt_pk_bf16_f32 v0, v19, v59
	ds_write_b32 v140, v0 offset:4172
	v_cvt_pk_bf16_f32 v0, v20, v60
	ds_write_b32 v140, v0 offset:5200
	v_cvt_pk_bf16_f32 v0, v21, v61
	ds_write_b32 v140, v0 offset:5204
	v_cvt_pk_bf16_f32 v0, v22, v62
	ds_write_b32 v140, v0 offset:5208
	v_cvt_pk_bf16_f32 v0, v23, v63
	ds_write_b32 v140, v0 offset:5212
	v_cvt_pk_bf16_f32 v0, v36, v40
	ds_write_b32 v140, v0 offset:6240
	v_cvt_pk_bf16_f32 v0, v37, v41
	ds_write_b32 v140, v0 offset:6244
	v_cvt_pk_bf16_f32 v0, v38, v42
	s_lshr_b32 s2, s21, 6
	ds_write_b32 v140, v0 offset:6248
	v_cvt_f32_u32_e32 v0, s2
	s_sub_i32 s30, 0, s2
	s_abs_i32 s29, s17
	s_ashr_i32 s21, s17, 31
	v_rcp_iflag_f32_e32 v0, v0
	v_cvt_pk_bf16_f32 v1, v39, v43
	ds_write_b32 v140, v1 offset:6252
	v_cvt_pk_bf16_f32 v1, v28, v24
	v_mul_f32_e32 v0, 0x4f7ffffe, v0
	v_cvt_u32_f32_e32 v0, v0
	ds_write_b32 v140, v1 offset:7280
	v_cvt_pk_bf16_f32 v1, v29, v25
	ds_write_b32 v140, v1 offset:7284
	v_readfirstlane_b32 s4, v0
	s_mul_i32 s30, s30, s4
	s_mul_hi_u32 s30, s4, s30
	s_add_i32 s4, s4, s30
	s_mul_hi_u32 s4, s29, s4
	s_mul_i32 s30, s4, s2
	s_sub_i32 s29, s29, s30
	s_add_i32 s30, s4, 1
	s_sub_i32 s31, s29, s2
	s_cmp_ge_u32 s29, s2
	s_cselect_b32 s4, s30, s4
	s_cselect_b32 s29, s31, s29
	s_add_i32 s30, s4, 1
	s_cmp_ge_u32 s29, s2
	s_cselect_b32 s4, s30, s4
	s_xor_b32 s4, s4, s21
	s_sub_i32 s4, s4, s21
	s_mul_i32 s2, s4, s2
	v_cvt_pk_bf16_f32 v1, v30, v26
	s_sub_i32 s2, s17, s2
	ds_write_b32 v140, v1 offset:7288
	v_cvt_pk_bf16_f32 v1, v31, v27
	ds_write_b32 v140, v1 offset:7292
	s_lshl_b32 s17, s2, 6
	s_ashr_i32 s2, s2, 2
	s_waitcnt lgkmcnt(0)
	s_mul_i32 s2, s2, s40
	s_add_i32 s4, s4, s41
	s_add_i32 s30, s4, s2
	ds_read2_b32 v[8:9], v134 offset1:8
	ds_read2_b32 v[0:1], v134 offset0:65 offset1:73
	ds_read2_b32 v[10:11], v134 offset0:130 offset1:138
	ds_read2_b32 v[2:3], v134 offset0:195 offset1:203
	s_ashr_i32 s31, s30, 31
	s_and_b32 s17, s17, 0xc0
	s_lshl_b64 s[30:31], s[30:31], 15
	s_add_u32 s14, s14, s30
	v_add_lshl_u32 v12, s17, v132, 6
	s_addc_u32 s15, s15, s31
	v_ashrrev_i32_e32 v13, 31, v12
	v_lshl_add_u64 v[12:13], v[12:13], 1, s[14:15]
	s_waitcnt lgkmcnt(3)
	v_mov_b32_e32 v4, v8
	s_waitcnt lgkmcnt(2)
	v_mov_b32_e32 v5, v0
	s_waitcnt lgkmcnt(1)
	v_mov_b32_e32 v6, v10
	s_waitcnt lgkmcnt(0)
	v_mov_b32_e32 v7, v2
	v_lshl_add_u64 v[12:13], v[12:13], 0, v[130:131]
	global_store_dwordx4 v[12:13], v[4:7], off
	v_mov_b32_e32 v0, v9
	v_mov_b32_e32 v2, v11
	v_add_lshl_u32 v4, s17, v135, 6
	v_ashrrev_i32_e32 v5, 31, v4
	v_lshl_add_u64 v[4:5], v[4:5], 1, s[14:15]
	v_lshl_add_u64 v[8:9], v[4:5], 0, v[130:131]
	ds_read2_b32 v[10:11], v134 offset0:16 offset1:24
	ds_read2_b32 v[4:5], v134 offset0:81 offset1:89
	ds_read2_b32 v[12:13], v134 offset0:146 offset1:154
	ds_read2_b32 v[6:7], v134 offset0:211 offset1:219
	global_store_dwordx4 v[8:9], v[0:3], off
	v_add_lshl_u32 v8, s17, v136, 6
	v_ashrrev_i32_e32 v9, 31, v8
	v_lshl_add_u64 v[8:9], v[8:9], 1, s[14:15]
	s_waitcnt lgkmcnt(3)
	v_mov_b32_e32 v0, v10
	s_waitcnt lgkmcnt(2)
	v_mov_b32_e32 v1, v4
	s_waitcnt lgkmcnt(1)
	v_mov_b32_e32 v2, v12
	s_waitcnt lgkmcnt(0)
	v_mov_b32_e32 v3, v6
	v_lshl_add_u64 v[8:9], v[8:9], 0, v[130:131]
	global_store_dwordx4 v[8:9], v[0:3], off
	v_mov_b32_e32 v4, v11
	v_mov_b32_e32 v6, v13
	v_add_lshl_u32 v0, s17, v137, 6
	v_ashrrev_i32_e32 v1, 31, v0
	v_lshl_add_u64 v[0:1], v[0:1], 1, s[14:15]
	v_lshl_add_u64 v[8:9], v[0:1], 0, v[130:131]
	ds_read2_b32 v[10:11], v134 offset0:32 offset1:40
	ds_read2_b32 v[0:1], v134 offset0:97 offset1:105
	ds_read2_b32 v[12:13], v134 offset0:162 offset1:170
	ds_read2_b32 v[2:3], v134 offset0:227 offset1:235
	global_store_dwordx4 v[8:9], v[4:7], off
	v_add_lshl_u32 v8, s17, v138, 6
	v_ashrrev_i32_e32 v9, 31, v8
	v_lshl_add_u64 v[8:9], v[8:9], 1, s[14:15]
	s_waitcnt lgkmcnt(3)
	v_mov_b32_e32 v4, v10
	s_waitcnt lgkmcnt(2)
	v_mov_b32_e32 v5, v0
	s_waitcnt lgkmcnt(1)
	v_mov_b32_e32 v6, v12
	s_waitcnt lgkmcnt(0)
	v_mov_b32_e32 v7, v2
	v_lshl_add_u64 v[8:9], v[8:9], 0, v[130:131]
	global_store_dwordx4 v[8:9], v[4:7], off
	v_mov_b32_e32 v0, v11
	v_mov_b32_e32 v2, v13
	v_add_lshl_u32 v4, s17, v139, 6
	v_ashrrev_i32_e32 v5, 31, v4
	v_lshl_add_u64 v[4:5], v[4:5], 1, s[14:15]
	v_lshl_add_u64 v[8:9], v[4:5], 0, v[130:131]
	ds_read2_b32 v[10:11], v134 offset0:48 offset1:56
	ds_read2_b32 v[4:5], v134 offset0:113 offset1:121
	ds_read2_b32 v[12:13], v134 offset0:178 offset1:186
	ds_read2_b32 v[6:7], v134 offset0:243 offset1:251
	global_store_dwordx4 v[8:9], v[0:3], off
	v_add_lshl_u32 v8, s17, v141, 6
	v_ashrrev_i32_e32 v9, 31, v8
	v_lshl_add_u64 v[8:9], v[8:9], 1, s[14:15]
	s_waitcnt lgkmcnt(3)
	v_mov_b32_e32 v0, v10
	s_waitcnt lgkmcnt(2)
	v_mov_b32_e32 v1, v4
	s_waitcnt lgkmcnt(1)
	v_mov_b32_e32 v2, v12
	s_waitcnt lgkmcnt(0)
	v_mov_b32_e32 v3, v6
	v_lshl_add_u64 v[8:9], v[8:9], 0, v[130:131]
	global_store_dwordx4 v[8:9], v[0:3], off
	v_mov_b32_e32 v4, v11
	v_mov_b32_e32 v6, v13
	v_add_lshl_u32 v0, s17, v142, 6
	v_ashrrev_i32_e32 v1, 31, v0
	v_lshl_add_u64 v[0:1], v[0:1], 1, s[14:15]
	v_lshl_add_u64 v[0:1], v[0:1], 0, v[130:131]
	global_store_dwordx4 v[0:1], v[4:7], off
	s_waitcnt lgkmcnt(0)
	s_add_i32 s22, s22, s25
	s_min_i32 s4, s22, s24
	s_cmpk_gt_i32 s4, 0x1fff
	s_mov_b64 s[34:35], -1
	s_cbranch_scc0 .LBB0_67
	s_cmpk_gt_u32 s4, 0x23ff
	s_cbranch_scc0 .LBB0_64
	s_cmpk_gt_u32 s4, 0x27ff
	s_cbranch_scc0 .LBB0_62
	s_cmpk_gt_u32 s4, 0x2bff
	s_cbranch_scc0 .LBB0_59
	s_cmp_gt_u32 s4, 0x12bff
	s_cbranch_scc0 .LBB0_56
	s_load_dwordx2 s[14:15], s[12:13], 0xa8
	s_add_i32 s2, s4, 0xfffed400
	s_lshr_b32 s2, s2, 10
	s_lshl_b64 s[30:31], s[2:3], 24
	s_mov_b64 s[34:35], 0
	s_waitcnt lgkmcnt(0)
	s_add_u32 s30, s14, s30
	s_addc_u32 s31, s15, s31
	s_lshl_b64 s[14:15], s[2:3], 23
	s_add_u32 s14, s18, s14
	s_addc_u32 s15, s19, s15
	s_and_b32 s17, s4, 0x3ff

; __device__ __forceinline__ unsigned cvt_pk_bf16(float lo, float hi) { unsigned r; asm volatile("v_cvt_pk_bf16_f32 %0, %1, %2" : "=v"(r) : "v"(lo), "v"(hi)); return r; }
; #define GAS __attribute__((address_space(1)))
; #define LAS __attribute__((address_space(3)))
; __device__ __forceinline__ void conv_load(const ConvSrc& c, int lane, f32x4 (&ra)[8], f32x4 (&rb)[8]) {
;     const int nblk = c.N >> 6, kb = c.kfast ? (c.item & 31) : c.item / nblk, nb = c.kfast ? (c.item >> 5) : c.item - kb * nblk, k0 = kb * 64, n0 = nb * 64;
;     const int n4 = (lane & 15) * 4, kq = lane >> 4;
; #pragma unroll
;     for (int i = 0; i < 8; ++i) { const int kp2 = 4 * i + kq; const float* p = c.W + (size_t)(k0 + 2 * kp2) * c.N + n0 + n4; ra[i] = __builtin_nontemporal_load((const GAS f32x4*)p); rb[i] = __builtin_nontemporal_load((const GAS f32x4*)(p + c.N)); }
; }
; __device__ __forceinline__ void conv_emit(const ConvSrc& c, int lane, LAS unsigned* P, const f32x4 (&ra)[8], const f32x4 (&rb)[8]) {
;     const int nblk = c.N >> 6, kb = c.kfast ? (c.item & 31) : c.item / nblk, nb = c.kfast ? (c.item >> 5) : c.item - kb * nblk, k0 = kb * 64, n0 = nb * 64;
;     const int n4 = (lane & 15) * 4, kq = lane >> 4;
; #pragma unroll
;     for (int i = 0; i < 8; ++i) { const int kp2 = 4 * i + kq; LAS unsigned* d = P + kp2 * 65 + n4;
;         d[0] = pg8::cvt_pk_bf16(ra[i].x, rb[i].x); d[1] = pg8::cvt_pk_bf16(ra[i].y, rb[i].y); d[2] = pg8::cvt_pk_bf16(ra[i].z, rb[i].z); d[3] = pg8::cvt_pk_bf16(ra[i].w, rb[i].w); }
.LBB0_614:
	s_lshr_b32 s4, s6, 6
	v_cvt_f32_u32_e32 v2, s4
	s_sub_i32 s63, 0, s4
	s_abs_i32 s62, s69
	s_ashr_i32 s59, s69, 31
	v_rcp_iflag_f32_e32 v2, v2
	v_mov_b32_e32 v135, v1
	v_mul_f32_e32 v2, 0x4f7ffffe, v2
	v_cvt_u32_f32_e32 v2, v2
	s_nop 0
	v_readfirstlane_b32 s64, v2
	s_mul_i32 s63, s63, s64
	s_mul_hi_u32 s63, s64, s63
	s_add_i32 s64, s64, s63
	s_mul_hi_u32 s63, s62, s64
	s_mul_i32 s64, s63, s4
	s_sub_i32 s62, s62, s64
	s_add_i32 s65, s63, 1
	s_sub_i32 s64, s62, s4
	s_cmp_ge_u32 s62, s4
	s_cselect_b32 s63, s65, s63
	s_cselect_b32 s62, s64, s62
	s_add_i32 s64, s63, 1
	s_cmp_ge_u32 s62, s4
	s_cselect_b32 s62, s64, s63
	s_xor_b32 s62, s62, s59
	s_sub_i32 s59, s62, s59
	v_lshl_add_u32 v52, s59, 6, v133
	s_mul_i32 s4, s59, s4
	v_mad_u64_u32 v[2:3], s[62:63], v52, s6, 0
	s_sub_i32 s4, s69, s4
	v_ashrrev_i32_e32 v5, 31, v52
	v_mov_b32_e32 v4, v3
	s_lshl_b32 s62, s4, 6
	v_mad_u64_u32 v[4:5], s[64:65], v5, s6, v[4:5]
	s_ashr_i32 s63, s62, 31
	v_mov_b32_e32 v3, v4
	s_waitcnt lgkmcnt(0)
	v_lshl_add_u64 v[2:3], v[2:3], 2, s[60:61]
	s_lshl_b64 s[62:63], s[62:63], 2
	v_lshl_add_u64 v[2:3], v[2:3], 0, s[62:63]
	v_lshl_add_u64 v[2:3], v[2:3], 0, v[0:1]
	s_lshl_b64 s[64:65], s[6:7], 2
	v_lshl_add_u64 v[6:7], v[2:3], 0, s[64:65]
	global_load_dwordx4 v[2:5], v[2:3], off nt
	s_nop 0
	global_load_dwordx4 v[26:29], v[6:7], off nt
	v_add_u32_e32 v6, 8, v52
	v_ashrrev_i32_e32 v9, 31, v6
	v_mad_u64_u32 v[6:7], vcc, v6, s6, 0
	v_mov_b32_e32 v8, v7
	v_mad_u64_u32 v[8:9], vcc, v9, s6, v[8:9]
	v_mov_b32_e32 v7, v8
	v_lshl_add_u64 v[6:7], v[6:7], 2, s[60:61]
	v_lshl_add_u64 v[6:7], v[6:7], 0, s[62:63]
	v_lshl_add_u64 v[6:7], v[6:7], 0, v[0:1]
	v_lshl_add_u64 v[10:11], v[6:7], 0, s[64:65]
	global_load_dwordx4 v[6:9], v[6:7], off nt
	s_nop 0
	global_load_dwordx4 v[34:37], v[10:11], off nt
	v_add_u32_e32 v10, 16, v52
	v_ashrrev_i32_e32 v13, 31, v10
	v_mad_u64_u32 v[10:11], vcc, v10, s6, 0
	v_mov_b32_e32 v12, v11
	v_mad_u64_u32 v[12:13], vcc, v13, s6, v[12:13]
	v_mov_b32_e32 v11, v12
	v_lshl_add_u64 v[10:11], v[10:11], 2, s[60:61]
	v_lshl_add_u64 v[10:11], v[10:11], 0, s[62:63]
	v_lshl_add_u64 v[10:11], v[10:11], 0, v[0:1]
	v_lshl_add_u64 v[14:15], v[10:11], 0, s[64:65]
	global_load_dwordx4 v[10:13], v[10:11], off nt
	s_nop 0
	global_load_dwordx4 v[30:33], v[14:15], off nt
	v_add_u32_e32 v14, 24, v52
	v_ashrrev_i32_e32 v17, 31, v14
	v_mad_u64_u32 v[14:15], vcc, v14, s6, 0
	v_mov_b32_e32 v16, v15
	v_mad_u64_u32 v[16:17], vcc, v17, s6, v[16:17]
	v_mov_b32_e32 v15, v16
	v_lshl_add_u64 v[14:15], v[14:15], 2, s[60:61]
	v_lshl_add_u64 v[14:15], v[14:15], 0, s[62:63]
	v_lshl_add_u64 v[14:15], v[14:15], 0, v[0:1]
	v_lshl_add_u64 v[18:19], v[14:15], 0, s[64:65]
	global_load_dwordx4 v[14:17], v[14:15], off nt
	s_nop 0
	global_load_dwordx4 v[42:45], v[18:19], off nt
	v_add_u32_e32 v18, 32, v52
	v_ashrrev_i32_e32 v21, 31, v18
	v_mad_u64_u32 v[18:19], vcc, v18, s6, 0
	v_mov_b32_e32 v20, v19
	v_mad_u64_u32 v[20:21], vcc, v21, s6, v[20:21]
	v_mov_b32_e32 v19, v20
	v_lshl_add_u64 v[18:19], v[18:19], 2, s[60:61]
	v_lshl_add_u64 v[18:19], v[18:19], 0, s[62:63]
	v_lshl_add_u64 v[18:19], v[18:19], 0, v[0:1]
	v_lshl_add_u64 v[22:23], v[18:19], 0, s[64:65]
	global_load_dwordx4 v[18:21], v[18:19], off nt
	s_nop 0
	global_load_dwordx4 v[38:41], v[22:23], off nt
	v_add_u32_e32 v22, 40, v52
	v_ashrrev_i32_e32 v25, 31, v22
	v_mad_u64_u32 v[22:23], vcc, v22, s6, 0
	v_mov_b32_e32 v24, v23
	v_mad_u64_u32 v[24:25], vcc, v25, s6, v[24:25]
	v_mov_b32_e32 v23, v24
	v_lshl_add_u64 v[22:23], v[22:23], 2, s[60:61]
	v_lshl_add_u64 v[22:23], v[22:23], 0, s[62:63]
	v_lshl_add_u64 v[22:23], v[22:23], 0, v[0:1]
	v_lshl_add_u64 v[46:47], v[22:23], 0, s[64:65]
	global_load_dwordx4 v[22:25], v[22:23], off nt
	s_nop 0
	global_load_dwordx4 v[62:65], v[46:47], off nt
	v_add_u32_e32 v46, 48, v52
	v_ashrrev_i32_e32 v49, 31, v46
	v_mad_u64_u32 v[46:47], vcc, v46, s6, 0
	v_mov_b32_e32 v48, v47
	v_mad_u64_u32 v[48:49], vcc, v49, s6, v[48:49]
	v_mov_b32_e32 v47, v48
	v_lshl_add_u64 v[46:47], v[46:47], 2, s[60:61]
	v_lshl_add_u64 v[46:47], v[46:47], 0, s[62:63]
	v_lshl_add_u64 v[46:47], v[46:47], 0, v[0:1]
	v_lshl_add_u64 v[50:51], v[46:47], 0, s[64:65]
	global_load_dwordx4 v[46:49], v[46:47], off nt
	s_nop 0
	global_load_dwordx4 v[58:61], v[50:51], off nt
	v_add_u32_e32 v50, 56, v52
	v_ashrrev_i32_e32 v53, 31, v50
	v_mad_u64_u32 v[50:51], vcc, v50, s6, 0
	v_mov_b32_e32 v52, v51
	v_mad_u64_u32 v[52:53], vcc, v53, s6, v[52:53]
	v_mov_b32_e32 v51, v52
	v_lshl_add_u64 v[50:51], v[50:51], 2, s[60:61]
	v_lshl_add_u64 v[50:51], v[50:51], 0, s[62:63]
	v_lshl_add_u64 v[50:51], v[50:51], 0, v[0:1]
	v_lshl_add_u64 v[52:53], v[50:51], 0, s[64:65]
	global_load_dwordx4 v[54:57], v[50:51], off nt
	s_nop 0
	global_load_dwordx4 v[50:53], v[52:53], off nt
	s_waitcnt vmcnt(38)
	v_cvt_pk_bf16_f32 v0, v66, v74
	ds_write_b32 v144, v0
	v_cvt_pk_bf16_f32 v0, v67, v75
	ds_write_b32 v144, v0 offset:4
	v_cvt_pk_bf16_f32 v0, v68, v76
	ds_write_b32 v144, v0 offset:8
	v_cvt_pk_bf16_f32 v0, v69, v77
	ds_write_b32 v144, v0 offset:12
	s_waitcnt vmcnt(36)
	v_cvt_pk_bf16_f32 v0, v70, v82
	ds_write_b32 v144, v0 offset:1040
	v_cvt_pk_bf16_f32 v0, v71, v83
	ds_write_b32 v144, v0 offset:1044
	v_cvt_pk_bf16_f32 v0, v72, v84
	ds_write_b32 v144, v0 offset:1048
	v_cvt_pk_bf16_f32 v0, v73, v85
	ds_write_b32 v144, v0 offset:1052
	s_waitcnt vmcnt(34)
; #define GAS __attribute__((address_space(1)))
; #define LAS __attribute__((address_space(3)))
; #define LDS_WAIT() asm volatile("s_waitcnt lgkmcnt(0)" ::: "memory")
; __device__ __forceinline__ void conv_emit(const ConvSrc& c, int lane, LAS unsigned* P, const f32x4 (&ra)[8], const f32x4 (&rb)[8]) {
;     ...
;     LDS_WAIT(); asm volatile("" ::: "memory");
;     const int cc = lane & 7;
; #pragma unroll
;     for (int jj = 0; jj < 8; ++jj) { const int n = (lane >> 3) + 8 * jj; const LAS unsigned* sp = P + (4 * cc) * 65 + n;
;         v4u o; o.x = sp[0]; o.y = sp[65]; o.z = sp[130]; o.w = sp[195];
;         bf16* dst = c.tiled ? c.WT + (size_t)((nb >> 2) * c.tiled + c.ktoff + kb) * 16384 + ((nb & 3) * 64 + n) * 64 + 8 * cc : c.WT + (size_t)(n0 + n) * c.ldk + k0 + 8 * cc;
;         __builtin_nontemporal_store(o, (GAS v4u*)dst); }
;     LDS_WAIT(); asm volatile("" ::: "memory");
	v_cvt_pk_bf16_f32 v0, v78, v90
	ds_write_b32 v144, v0 offset:2080
	v_cvt_pk_bf16_f32 v0, v79, v91
	ds_write_b32 v144, v0 offset:2084
	v_cvt_pk_bf16_f32 v0, v80, v92
	ds_write_b32 v144, v0 offset:2088
	v_cvt_pk_bf16_f32 v0, v81, v93
	ds_write_b32 v144, v0 offset:2092
	s_waitcnt vmcnt(32)
	v_cvt_pk_bf16_f32 v0, v86, v98
	ds_write_b32 v144, v0 offset:3120
	v_cvt_pk_bf16_f32 v0, v87, v99
	ds_write_b32 v144, v0 offset:3124
	v_cvt_pk_bf16_f32 v0, v88, v100
	ds_write_b32 v144, v0 offset:3128
	v_cvt_pk_bf16_f32 v0, v89, v101
	ds_write_b32 v144, v0 offset:3132
	s_waitcnt vmcnt(30)
	v_cvt_pk_bf16_f32 v0, v94, v106
	ds_write_b32 v144, v0 offset:4160
	v_cvt_pk_bf16_f32 v0, v95, v107
	ds_write_b32 v144, v0 offset:4164
	v_cvt_pk_bf16_f32 v0, v96, v108
	ds_write_b32 v144, v0 offset:4168
	v_cvt_pk_bf16_f32 v0, v97, v109
	ds_write_b32 v144, v0 offset:4172
	s_waitcnt vmcnt(28)
	v_cvt_pk_bf16_f32 v0, v102, v114
	ds_write_b32 v144, v0 offset:5200
	v_cvt_pk_bf16_f32 v0, v103, v115
	ds_write_b32 v144, v0 offset:5204
	v_cvt_pk_bf16_f32 v0, v104, v116
	ds_write_b32 v144, v0 offset:5208
	v_cvt_pk_bf16_f32 v0, v105, v117
	ds_write_b32 v144, v0 offset:5212
	s_waitcnt vmcnt(26)
	v_cvt_pk_bf16_f32 v0, v110, v126
	ds_write_b32 v144, v0 offset:6240
	v_cvt_pk_bf16_f32 v0, v111, v127
	ds_write_b32 v144, v0 offset:6244
	v_cvt_pk_bf16_f32 v0, v112, v128
	ds_write_b32 v144, v0 offset:6248
	v_cvt_pk_bf16_f32 v0, v113, v129
	ds_write_b32 v144, v0 offset:6252
	s_waitcnt vmcnt(24)
	v_cvt_pk_bf16_f32 v0, v118, v122
	ds_write_b32 v144, v0 offset:7280
	v_cvt_pk_bf16_f32 v0, v119, v123
	ds_write_b32 v144, v0 offset:7284
	v_cvt_pk_bf16_f32 v0, v120, v124
	ds_write_b32 v144, v0 offset:7288
	v_cvt_pk_bf16_f32 v0, v121, v125
	ds_write_b32 v144, v0 offset:7292
	s_ashr_i32 s4, s21, 2
	s_waitcnt lgkmcnt(0)
	s_mul_i32 s4, s4, s5
	s_add_i32 s5, s20, s19
	s_add_i32 s4, s5, s4
	ds_read2_b32 v[74:75], v136 offset1:8
	ds_read2_b32 v[66:67], v136 offset0:65 offset1:73
	ds_read2_b32 v[76:77], v136 offset0:130 offset1:138
	ds_read2_b32 v[68:69], v136 offset0:195 offset1:203
	s_ashr_i32 s5, s4, 31
	s_and_b32 s21, s58, 0xc0
	s_lshl_b64 s[4:5], s[4:5], 15
	s_add_u32 s56, s56, s4
	v_add_lshl_u32 v78, s21, v131, 6
	s_addc_u32 s57, s57, s5
	v_ashrrev_i32_e32 v79, 31, v78
	v_lshl_add_u64 v[78:79], v[78:79], 1, s[56:57]
	s_waitcnt lgkmcnt(3)
	v_mov_b32_e32 v70, v74
	s_waitcnt lgkmcnt(2)
	v_mov_b32_e32 v71, v66
	s_waitcnt lgkmcnt(1)
	v_mov_b32_e32 v72, v76
	s_waitcnt lgkmcnt(0)
	v_mov_b32_e32 v73, v68
	v_lshl_add_u64 v[78:79], v[78:79], 0, v[134:135]
	global_store_dwordx4 v[78:79], v[70:73], off
	v_mov_b32_e32 v66, v75
	v_mov_b32_e32 v68, v77
	v_add_lshl_u32 v70, s21, v137, 6
	v_ashrrev_i32_e32 v71, 31, v70
	v_lshl_add_u64 v[70:71], v[70:71], 1, s[56:57]
	v_lshl_add_u64 v[74:75], v[70:71], 0, v[134:135]
	ds_read2_b32 v[76:77], v136 offset0:16 offset1:24
	ds_read2_b32 v[70:71], v136 offset0:81 offset1:89
	ds_read2_b32 v[78:79], v136 offset0:146 offset1:154
	ds_read2_b32 v[72:73], v136 offset0:211 offset1:219
	global_store_dwordx4 v[74:75], v[66:69], off
	v_add_lshl_u32 v74, s21, v138, 6
	v_ashrrev_i32_e32 v75, 31, v74
	v_lshl_add_u64 v[74:75], v[74:75], 1, s[56:57]
	s_waitcnt lgkmcnt(3)
	v_mov_b32_e32 v66, v76
	s_waitcnt lgkmcnt(2)
	v_mov_b32_e32 v67, v70
	s_waitcnt lgkmcnt(1)
	v_mov_b32_e32 v68, v78
	s_waitcnt lgkmcnt(0)
	v_mov_b32_e32 v69, v72
	v_lshl_add_u64 v[74:75], v[74:75], 0, v[134:135]
	global_store_dwordx4 v[74:75], v[66:69], off
	v_mov_b32_e32 v70, v77
	v_mov_b32_e32 v72, v79
	v_add_lshl_u32 v66, s21, v139, 6
	v_ashrrev_i32_e32 v67, 31, v66
	v_lshl_add_u64 v[66:67], v[66:67], 1, s[56:57]
	v_lshl_add_u64 v[74:75], v[66:67], 0, v[134:135]
	ds_read2_b32 v[76:77], v136 offset0:32 offset1:40
	ds_read2_b32 v[66:67], v136 offset0:97 offset1:105
	ds_read2_b32 v[78:79], v136 offset0:162 offset1:170
	ds_read2_b32 v[68:69], v136 offset0:227 offset1:235
	global_store_dwordx4 v[74:75], v[70:73], off
	v_add_lshl_u32 v74, s21, v140, 6
	v_ashrrev_i32_e32 v75, 31, v74
	v_lshl_add_u64 v[74:75], v[74:75], 1, s[56:57]
	s_waitcnt lgkmcnt(3)
	v_mov_b32_e32 v70, v76
	s_waitcnt lgkmcnt(2)
	v_mov_b32_e32 v71, v66
	s_waitcnt lgkmcnt(1)
	v_mov_b32_e32 v72, v78
	s_waitcnt lgkmcnt(0)
	v_mov_b32_e32 v73, v68
	v_lshl_add_u64 v[74:75], v[74:75], 0, v[134:135]
	global_store_dwordx4 v[74:75], v[70:73], off
	v_mov_b32_e32 v66, v77
	v_mov_b32_e32 v68, v79
	v_add_lshl_u32 v70, s21, v141, 6
	v_ashrrev_i32_e32 v71, 31, v70
	v_lshl_add_u64 v[70:71], v[70:71], 1, s[56:57]
	v_lshl_add_u64 v[74:75], v[70:71], 0, v[134:135]
	ds_read2_b32 v[76:77], v136 offset0:48 offset1:56
	ds_read2_b32 v[70:71], v136 offset0:113 offset1:121
	ds_read2_b32 v[78:79], v136 offset0:178 offset1:186
	ds_read2_b32 v[72:73], v136 offset0:243 offset1:251
	global_store_dwordx4 v[74:75], v[66:69], off
	v_add_lshl_u32 v74, s21, v142, 6
	v_ashrrev_i32_e32 v75, 31, v74
	v_lshl_add_u64 v[74:75], v[74:75], 1, s[56:57]
	s_waitcnt lgkmcnt(3)
	v_mov_b32_e32 v66, v76
	s_waitcnt lgkmcnt(2)
	v_mov_b32_e32 v67, v70
	s_waitcnt lgkmcnt(1)
	v_mov_b32_e32 v68, v78
	s_waitcnt lgkmcnt(0)
	v_mov_b32_e32 v69, v72
	v_lshl_add_u64 v[74:75], v[74:75], 0, v[134:135]
	global_store_dwordx4 v[74:75], v[66:69], off
	v_mov_b32_e32 v70, v77
	v_mov_b32_e32 v72, v79
	v_add_lshl_u32 v66, s21, v143, 6
	v_ashrrev_i32_e32 v67, 31, v66
	v_lshl_add_u64 v[66:67], v[66:67], 1, s[56:57]
	v_lshl_add_u64 v[66:67], v[66:67], 0, v[134:135]
	global_store_dwordx4 v[66:67], v[70:73], off
	s_waitcnt lgkmcnt(0)
	s_cmp_lt_i32 s23, 0x12c00
	s_mov_b32 s4, s6
	s_cbranch_scc0 .LBB0_321

; #define GAS __attribute__((address_space(1)))
; __device__ __forceinline__ void conv_load(const ConvSrc& c, int lane, f32x4 (&ra)[8], f32x4 (&rb)[8]) {
;     const int nblk = c.N >> 6, kb = c.kfast ? (c.item & 31) : c.item / nblk, nb = c.kfast ? (c.item >> 5) : c.item - kb * nblk, k0 = kb * 64, n0 = nb * 64;
;     const int n4 = (lane & 15) * 4, kq = lane >> 4;
; #pragma unroll
;     for (int i = 0; i < 8; ++i) { const int kp2 = 4 * i + kq; const float* p = c.W + (size_t)(k0 + 2 * kp2) * c.N + n0 + n4; ra[i] = __builtin_nontemporal_load((const GAS f32x4*)p); rb[i] = __builtin_nontemporal_load((const GAS f32x4*)(p + c.N)); }
; }
.LBB0_634:
	s_lshr_b32 s58, s6, 6
	v_cvt_f32_u32_e32 v0, s58
	s_sub_i32 s62, 0, s58
	s_abs_i32 s59, s21
	s_ashr_i32 s20, s21, 31
	v_rcp_iflag_f32_e32 v0, v0
	v_mov_b32_e32 v135, v1
	v_mul_f32_e32 v0, 0x4f7ffffe, v0
	v_cvt_u32_f32_e32 v0, v0
	s_nop 0
	v_readfirstlane_b32 s63, v0
	s_mul_i32 s62, s62, s63
	s_mul_hi_u32 s62, s63, s62
	s_add_i32 s63, s63, s62
	s_mul_hi_u32 s62, s59, s63
	s_mul_i32 s63, s62, s58
	s_sub_i32 s59, s59, s63
	s_add_i32 s63, s62, 1
	s_sub_i32 s64, s59, s58
	s_cmp_ge_u32 s59, s58
	s_cselect_b32 s62, s63, s62
	s_cselect_b32 s59, s64, s59
	s_add_i32 s63, s62, 1
	s_cmp_ge_u32 s59, s58
	s_cselect_b32 s59, s63, s62
	s_xor_b32 s59, s59, s20
	s_sub_i32 s20, s59, s20
	v_lshl_add_u32 v120, s20, 6, v133
	s_mul_i32 s58, s20, s58
	v_mad_u64_u32 v[66:67], s[62:63], v120, s6, 0
	s_sub_i32 s21, s21, s58
	v_ashrrev_i32_e32 v68, 31, v120
	v_mov_b32_e32 v0, v67
	s_lshl_b32 s58, s21, 6
	v_mad_u64_u32 v[68:69], s[62:63], v68, s6, v[0:1]
	s_ashr_i32 s59, s58, 31
	v_mov_b32_e32 v67, v68
	s_waitcnt lgkmcnt(0)
	v_lshl_add_u64 v[66:67], v[66:67], 2, s[60:61]
	s_lshl_b64 s[62:63], s[58:59], 2
	v_lshl_add_u64 v[66:67], v[66:67], 0, s[62:63]
	v_lshlrev_b32_e32 v0, 2, v130
	v_lshl_add_u64 v[70:71], v[66:67], 0, v[0:1]
	s_lshl_b64 s[64:65], s[6:7], 2
	global_load_dwordx4 v[66:69], v[70:71], off nt
	v_lshl_add_u64 v[70:71], v[70:71], 0, s[64:65]
	global_load_dwordx4 v[74:77], v[70:71], off nt
	v_add_u32_e32 v70, 8, v120
	v_ashrrev_i32_e32 v73, 31, v70
	v_mad_u64_u32 v[70:71], vcc, v70, s6, 0
	v_mov_b32_e32 v72, v71
	v_mad_u64_u32 v[72:73], vcc, v73, s6, v[72:73]
	v_mov_b32_e32 v71, v72
	v_lshl_add_u64 v[70:71], v[70:71], 2, s[60:61]
	v_lshl_add_u64 v[70:71], v[70:71], 0, s[62:63]
	v_lshl_add_u64 v[78:79], v[70:71], 0, v[0:1]
	global_load_dwordx4 v[70:73], v[78:79], off nt
	v_lshl_add_u64 v[78:79], v[78:79], 0, s[64:65]
	global_load_dwordx4 v[82:85], v[78:79], off nt
	v_add_u32_e32 v78, 16, v120
	v_ashrrev_i32_e32 v81, 31, v78
	v_mad_u64_u32 v[78:79], vcc, v78, s6, 0
	v_mov_b32_e32 v80, v79
	v_mad_u64_u32 v[80:81], vcc, v81, s6, v[80:81]
	v_mov_b32_e32 v79, v80
	v_lshl_add_u64 v[78:79], v[78:79], 2, s[60:61]
	v_lshl_add_u64 v[78:79], v[78:79], 0, s[62:63]
	v_lshl_add_u64 v[86:87], v[78:79], 0, v[0:1]
	global_load_dwordx4 v[78:81], v[86:87], off nt
	v_lshl_add_u64 v[86:87], v[86:87], 0, s[64:65]
	global_load_dwordx4 v[90:93], v[86:87], off nt
	v_add_u32_e32 v86, 24, v120
	v_ashrrev_i32_e32 v89, 31, v86
	v_mad_u64_u32 v[86:87], vcc, v86, s6, 0
	v_mov_b32_e32 v88, v87
	v_mad_u64_u32 v[88:89], vcc, v89, s6, v[88:89]
	v_mov_b32_e32 v87, v88
	v_lshl_add_u64 v[86:87], v[86:87], 2, s[60:61]
	v_lshl_add_u64 v[86:87], v[86:87], 0, s[62:63]
	v_lshl_add_u64 v[94:95], v[86:87], 0, v[0:1]
	global_load_dwordx4 v[86:89], v[94:95], off nt
	v_lshl_add_u64 v[94:95], v[94:95], 0, s[64:65]
	global_load_dwordx4 v[98:101], v[94:95], off nt
	v_add_u32_e32 v94, 32, v120
	v_ashrrev_i32_e32 v97, 31, v94
	v_mad_u64_u32 v[94:95], vcc, v94, s6, 0
	v_mov_b32_e32 v96, v95
	v_mad_u64_u32 v[96:97], vcc, v97, s6, v[96:97]
	v_mov_b32_e32 v95, v96
	v_lshl_add_u64 v[94:95], v[94:95], 2, s[60:61]
	v_lshl_add_u64 v[94:95], v[94:95], 0, s[62:63]
	v_lshl_add_u64 v[102:103], v[94:95], 0, v[0:1]
	global_load_dwordx4 v[94:97], v[102:103], off nt
	v_lshl_add_u64 v[102:103], v[102:103], 0, s[64:65]
	global_load_dwordx4 v[106:109], v[102:103], off nt
	v_add_u32_e32 v102, 40, v120
	v_ashrrev_i32_e32 v105, 31, v102
	v_mad_u64_u32 v[102:103], vcc, v102, s6, 0
	v_mov_b32_e32 v104, v103
	v_mad_u64_u32 v[104:105], vcc, v105, s6, v[104:105]
	v_mov_b32_e32 v103, v104
	v_lshl_add_u64 v[102:103], v[102:103], 2, s[60:61]
	v_lshl_add_u64 v[102:103], v[102:103], 0, s[62:63]
	v_lshl_add_u64 v[110:111], v[102:103], 0, v[0:1]
	global_load_dwordx4 v[102:105], v[110:111], off nt
	v_lshl_add_u64 v[110:111], v[110:111], 0, s[64:65]
	global_load_dwordx4 v[114:117], v[110:111], off nt
	v_add_u32_e32 v110, 48, v120
	v_ashrrev_i32_e32 v113, 31, v110
	v_mad_u64_u32 v[110:111], vcc, v110, s6, 0
	v_mov_b32_e32 v112, v111
	v_mad_u64_u32 v[112:113], vcc, v113, s6, v[112:113]
	v_mov_b32_e32 v111, v112
	v_lshl_add_u64 v[110:111], v[110:111], 2, s[60:61]
	v_lshl_add_u64 v[110:111], v[110:111], 0, s[62:63]
	v_lshl_add_u64 v[118:119], v[110:111], 0, v[0:1]
	global_load_dwordx4 v[110:113], v[118:119], off nt
	v_lshl_add_u64 v[118:119], v[118:119], 0, s[64:65]
	global_load_dwordx4 v[126:129], v[118:119], off nt
	v_add_u32_e32 v118, 56, v120
	v_ashrrev_i32_e32 v121, 31, v118
	v_mad_u64_u32 v[118:119], vcc, v118, s6, 0
	v_mov_b32_e32 v120, v119
	v_mad_u64_u32 v[120:121], vcc, v121, s6, v[120:121]
	v_mov_b32_e32 v119, v120
	v_lshl_add_u64 v[118:119], v[118:119], 2, s[60:61]
	v_lshl_add_u64 v[118:119], v[118:119], 0, s[62:63]
	v_lshl_add_u64 v[122:123], v[118:119], 0, v[0:1]
	global_load_dwordx4 v[118:121], v[122:123], off nt
	v_lshl_add_u64 v[122:123], v[122:123], 0, s[64:65]
	global_load_dwordx4 v[122:125], v[122:123], off nt
	s_lshr_b32 s4, s4, 6
	s_waitcnt vmcnt(16)
; #define GAS __attribute__((address_space(1)))
; #define LAS __attribute__((address_space(3)))
; __device__ __forceinline__ ConvSrc conv_decode(KP kp, unsigned char* ws, int it) {
;     constexpr int I_IN = 32 * 256, I_SQ = 32 * 32, I_UP = 32 * 64, I_DN = 32 * 32;
;     ConvSrc c; int r = it; c.ldk = 2048; c.kfast = 0; c.tiled = 32; c.ktoff = 0;
;     if (r < I_IN) { c.W = (const float*)KIN(6); c.WT = (bf16*)(ws + WS_WIN); c.N = 16384; c.item = r; return c; } r -= I_IN;
;     if (r < I_SQ) { c.W = (const float*)KIN(13); c.WT = (bf16*)(ws + WS_WAO); c.N = 2048; c.item = r; c.ldk = 4096; c.tiled = 64; return c; } r -= I_SQ;
;     if (r < I_SQ) { c.W = (const float*)KIN(14); c.WT = (bf16*)(ws + WS_WAO); c.N = 2048; c.item = r; c.ldk = 4096; c.tiled = 64; c.ktoff = 32; return c; } r -= I_SQ;
;     if (r < I_SQ) { c.W = (const float*)KIN(15); c.WT = (bf16*)(ws + WS_WO); c.N = 2048; c.item = r; return c; } r -= I_SQ;
;     if (r < NE * I_UP) { const int e = r / I_UP; c.W = (const float*)KIN(19) + (size_t)e * 2048 * 4096; c.WT = (bf16*)(ws + WS_WUP) + (size_t)e * 4096 * 2048; c.N = 4096; c.item = r - e * I_UP; return c; } r -= NE * I_UP;
; __device__ __forceinline__ void conv_emit(const ConvSrc& c, int lane, LAS unsigned* P, const f32x4 (&ra)[8], const f32x4 (&rb)[8]) {
;     const int nblk = c.N >> 6, kb = c.kfast ? (c.item & 31) : c.item / nblk, nb = c.kfast ? (c.item >> 5) : c.item - kb * nblk, k0 = kb * 64, n0 = nb * 64;
;     const int n4 = (lane & 15) * 4, kq = lane >> 4;
; #pragma unroll
;     for (int i = 0; i < 8; ++i) { const int kp2 = 4 * i + kq; LAS unsigned* d = P + kp2 * 65 + n4;
;         d[0] = pg8::cvt_pk_bf16(ra[i].x, rb[i].x); d[1] = pg8::cvt_pk_bf16(ra[i].y, rb[i].y); d[2] = pg8::cvt_pk_bf16(ra[i].z, rb[i].z); d[3] = pg8::cvt_pk_bf16(ra[i].w, rb[i].w); }
;     LDS_WAIT(); asm volatile("" ::: "memory");
;     const int cc = lane & 7;
; #pragma unroll
;     for (int jj = 0; jj < 8; ++jj) { const int n = (lane >> 3) + 8 * jj; const LAS unsigned* sp = P + (4 * cc) * 65 + n;
;         v4u o; o.x = sp[0]; o.y = sp[65]; o.z = sp[130]; o.w = sp[195];
;         bf16* dst = c.tiled ? c.WT + (size_t)((nb >> 2) * c.tiled + c.ktoff + kb) * 16384 + ((nb & 3) * 64 + n) * 64 + 8 * cc : c.WT + (size_t)(n0 + n) * c.ldk + k0 + 8 * cc;
;         __builtin_nontemporal_store(o, (GAS v4u*)dst); }
;     LDS_WAIT(); asm volatile("" ::: "memory");
	v_cvt_pk_bf16_f32 v2, v2, v26
	v_cvt_f32_u32_e32 v134, s4
	ds_write_b32 v144, v2
	v_cvt_pk_bf16_f32 v2, v3, v27
	ds_write_b32 v144, v2 offset:4
	v_cvt_pk_bf16_f32 v2, v4, v28
	ds_write_b32 v144, v2 offset:8
	v_cvt_pk_bf16_f32 v2, v5, v29
	ds_write_b32 v144, v2 offset:12
	v_cvt_pk_bf16_f32 v2, v6, v34
	v_rcp_iflag_f32_e32 v134, v134
	ds_write_b32 v144, v2 offset:1040
	v_cvt_pk_bf16_f32 v2, v7, v35
	ds_write_b32 v144, v2 offset:1044
	v_cvt_pk_bf16_f32 v2, v8, v36
	ds_write_b32 v144, v2 offset:1048
	v_cvt_pk_bf16_f32 v2, v9, v37
	ds_write_b32 v144, v2 offset:1052
	v_cvt_pk_bf16_f32 v2, v10, v30
	v_mul_f32_e32 v134, 0x4f7ffffe, v134
	ds_write_b32 v144, v2 offset:2080
	v_cvt_pk_bf16_f32 v2, v11, v31
	v_cvt_u32_f32_e32 v134, v134
	ds_write_b32 v144, v2 offset:2084
	v_cvt_pk_bf16_f32 v2, v12, v32
	ds_write_b32 v144, v2 offset:2088
	v_cvt_pk_bf16_f32 v2, v13, v33
	ds_write_b32 v144, v2 offset:2092
	v_cvt_pk_bf16_f32 v2, v14, v42
	ds_write_b32 v144, v2 offset:3120
	v_cvt_pk_bf16_f32 v2, v15, v43
	s_sub_i32 s60, 0, s4
	v_readfirstlane_b32 s61, v134
	ds_write_b32 v144, v2 offset:3124
	v_cvt_pk_bf16_f32 v2, v16, v44
	s_mul_i32 s60, s60, s61
	ds_write_b32 v144, v2 offset:3128
	v_cvt_pk_bf16_f32 v2, v17, v45
	s_mul_hi_u32 s60, s61, s60
	ds_write_b32 v144, v2 offset:3132
	v_cvt_pk_bf16_f32 v2, v18, v38
	s_abs_i32 s59, s69
	s_add_i32 s61, s61, s60
	ds_write_b32 v144, v2 offset:4160
	v_cvt_pk_bf16_f32 v2, v19, v39
	s_mul_hi_u32 s60, s59, s61
	ds_write_b32 v144, v2 offset:4164
	v_cvt_pk_bf16_f32 v2, v20, v40
	s_mul_i32 s61, s60, s4
	ds_write_b32 v144, v2 offset:4168
	v_cvt_pk_bf16_f32 v2, v21, v41
	s_sub_i32 s59, s59, s61
	ds_write_b32 v144, v2 offset:4172
	v_cvt_pk_bf16_f32 v2, v22, v62
	s_ashr_i32 s6, s69, 31
	s_add_i32 s61, s60, 1
	s_sub_i32 s62, s59, s4
	ds_write_b32 v144, v2 offset:5200
	v_cvt_pk_bf16_f32 v2, v23, v63
	s_cmp_ge_u32 s59, s4
	ds_write_b32 v144, v2 offset:5204
	v_cvt_pk_bf16_f32 v2, v24, v64
	s_cselect_b32 s60, s61, s60
	ds_write_b32 v144, v2 offset:5208
	v_cvt_pk_bf16_f32 v2, v25, v65
	s_cselect_b32 s59, s62, s59
	s_add_i32 s61, s60, 1
	ds_write_b32 v144, v2 offset:5212
	v_cvt_pk_bf16_f32 v2, v46, v58
	s_cmp_ge_u32 s59, s4
	ds_write_b32 v144, v2 offset:6240
	v_cvt_pk_bf16_f32 v2, v47, v59
	s_cselect_b32 s59, s61, s60
	ds_write_b32 v144, v2 offset:6244
	v_cvt_pk_bf16_f32 v2, v48, v60
	s_xor_b32 s59, s59, s6
	ds_write_b32 v144, v2 offset:6248
	v_cvt_pk_bf16_f32 v2, v49, v61
	s_sub_i32 s6, s59, s6
	ds_write_b32 v144, v2 offset:6252
	v_cvt_pk_bf16_f32 v2, v54, v50
	s_mul_i32 s4, s6, s4
	ds_write_b32 v144, v2 offset:7280
	v_cvt_pk_bf16_f32 v2, v55, v51
	s_sub_i32 s4, s69, s4
	ds_write_b32 v144, v2 offset:7284
	v_cvt_pk_bf16_f32 v2, v56, v52
	ds_write_b32 v144, v2 offset:7288
	v_cvt_pk_bf16_f32 v2, v57, v53
	ds_write_b32 v144, v2 offset:7292
	s_ashr_i32 s60, s4, 2
	s_waitcnt lgkmcnt(0)
	s_mul_i32 s60, s60, s17
	s_add_i32 s6, s6, s66
	s_add_i32 s60, s6, s60
	s_lshl_b32 s59, s4, 6
	ds_read2_b32 v[2:3], v136 offset0:65 offset1:73
	ds_read2_b32 v[10:11], v136 offset0:130 offset1:138
	ds_read2_b32 v[4:5], v136 offset0:195 offset1:203
	ds_read2_b32 v[12:13], v136 offset1:8
	s_ashr_i32 s61, s60, 31
	s_and_b32 s4, s59, 0xc0
	s_lshl_b64 s[60:61], s[60:61], 15
	s_add_u32 s54, s54, s60
	v_add_lshl_u32 v14, s4, v131, 6
	s_addc_u32 s55, s55, s61
	v_ashrrev_i32_e32 v15, 31, v14
	v_lshl_add_u64 v[14:15], v[14:15], 1, s[54:55]
	v_lshlrev_b32_e32 v134, 1, v132
	s_waitcnt lgkmcnt(0)
	v_mov_b32_e32 v6, v12
	v_mov_b32_e32 v7, v2
	v_mov_b32_e32 v8, v10
	v_mov_b32_e32 v9, v4
	v_lshl_add_u64 v[14:15], v[14:15], 0, v[134:135]
	global_store_dwordx4 v[14:15], v[6:9], off
	v_mov_b32_e32 v2, v13
	v_mov_b32_e32 v4, v11
	v_add_lshl_u32 v6, s4, v137, 6
	v_ashrrev_i32_e32 v7, 31, v6
	v_lshl_add_u64 v[6:7], v[6:7], 1, s[54:55]
	v_lshl_add_u64 v[6:7], v[6:7], 0, v[134:135]
	global_store_dwordx4 v[6:7], v[2:5], off
	ds_read2_b32 v[10:11], v136 offset0:16 offset1:24
	ds_read2_b32 v[2:3], v136 offset0:81 offset1:89
	ds_read2_b32 v[12:13], v136 offset0:146 offset1:154
	ds_read2_b32 v[4:5], v136 offset0:211 offset1:219
	v_add_lshl_u32 v14, s4, v138, 6
	v_ashrrev_i32_e32 v15, 31, v14
	v_lshl_add_u64 v[14:15], v[14:15], 1, s[54:55]
	s_waitcnt lgkmcnt(3)
	v_mov_b32_e32 v6, v10
	s_waitcnt lgkmcnt(2)
	v_mov_b32_e32 v7, v2
	s_waitcnt lgkmcnt(1)
	v_mov_b32_e32 v8, v12
	s_waitcnt lgkmcnt(0)
	v_mov_b32_e32 v9, v4
	v_lshl_add_u64 v[14:15], v[14:15], 0, v[134:135]
	global_store_dwordx4 v[14:15], v[6:9], off
	v_mov_b32_e32 v2, v11
	v_mov_b32_e32 v4, v13
	v_add_lshl_u32 v6, s4, v139, 6
	v_ashrrev_i32_e32 v7, 31, v6
	v_lshl_add_u64 v[6:7], v[6:7], 1, s[54:55]
	v_lshl_add_u64 v[6:7], v[6:7], 0, v[134:135]
	global_store_dwordx4 v[6:7], v[2:5], off
	ds_read2_b32 v[2:3], v136 offset0:97 offset1:105
	ds_read2_b32 v[10:11], v136 offset0:162 offset1:170
	ds_read2_b32 v[4:5], v136 offset0:227 offset1:235
	ds_read2_b32 v[12:13], v136 offset0:32 offset1:40
	v_add_lshl_u32 v14, s4, v140, 6
	v_ashrrev_i32_e32 v15, 31, v14
	v_lshl_add_u64 v[14:15], v[14:15], 1, s[54:55]
	s_waitcnt lgkmcnt(3)
	v_mov_b32_e32 v7, v2
	s_waitcnt lgkmcnt(0)
	v_mov_b32_e32 v6, v12
	v_mov_b32_e32 v8, v10
	v_mov_b32_e32 v9, v4
	v_lshl_add_u64 v[14:15], v[14:15], 0, v[134:135]
	global_store_dwordx4 v[14:15], v[6:9], off
	v_mov_b32_e32 v2, v13
	v_mov_b32_e32 v4, v11
	v_add_lshl_u32 v6, s4, v141, 6
	v_ashrrev_i32_e32 v7, 31, v6
	v_lshl_add_u64 v[6:7], v[6:7], 1, s[54:55]
	v_lshl_add_u64 v[6:7], v[6:7], 0, v[134:135]
	global_store_dwordx4 v[6:7], v[2:5], off
	ds_read2_b32 v[10:11], v136 offset0:48 offset1:56
	ds_read2_b32 v[2:3], v136 offset0:113 offset1:121
	ds_read2_b32 v[12:13], v136 offset0:178 offset1:186
	ds_read2_b32 v[4:5], v136 offset0:243 offset1:251
	v_add_lshl_u32 v14, s4, v142, 6
	v_ashrrev_i32_e32 v15, 31, v14
	v_lshl_add_u64 v[14:15], v[14:15], 1, s[54:55]
	s_waitcnt lgkmcnt(3)
	v_mov_b32_e32 v6, v10
	s_waitcnt lgkmcnt(2)
	v_mov_b32_e32 v7, v2
	s_waitcnt lgkmcnt(1)
	v_mov_b32_e32 v8, v12
	s_waitcnt lgkmcnt(0)
	v_mov_b32_e32 v9, v4
	v_lshl_add_u64 v[14:15], v[14:15], 0, v[134:135]
	global_store_dwordx4 v[14:15], v[6:9], off
	v_mov_b32_e32 v2, v11
	v_mov_b32_e32 v4, v13
	v_add_lshl_u32 v6, s4, v143, 6
	v_ashrrev_i32_e32 v7, 31, v6
	v_lshl_add_u64 v[6:7], v[6:7], 1, s[54:55]
	v_lshl_add_u64 v[6:7], v[6:7], 0, v[134:135]
	global_store_dwordx4 v[6:7], v[2:5], off
	s_waitcnt lgkmcnt(0)
	s_add_i32 s23, s23, s73
	s_min_i32 s4, s23, s88
	s_mov_b64 s[62:63], -1
	s_cmpk_gt_i32 s4, 0x1fff
	s_cbranch_scc0 .LBB0_651
	s_cmpk_gt_u32 s4, 0x23ff
	s_cbranch_scc0 .LBB0_648
	s_cmpk_gt_u32 s4, 0x27ff
	s_cbranch_scc0 .LBB0_646
	s_cmpk_gt_u32 s4, 0x2bff
	s_cbranch_scc0 .LBB0_643
	s_cmp_gt_u32 s4, 0x12bff
	s_cbranch_scc0 .LBB0_640
	s_load_dwordx2 s[54:55], s[2:3], 0xa8
	s_add_i32 s6, s4, 0xfffed400
	s_lshr_b32 s6, s6, 10
	s_lshl_b64 s[60:61], s[6:7], 24
	s_mov_b64 s[62:63], 0
	s_waitcnt lgkmcnt(0)
	s_add_u32 s60, s54, s60
	s_addc_u32 s61, s55, s61
	s_lshl_b64 s[54:55], s[6:7], 23
	s_add_u32 s54, s84, s54
	s_addc_u32 s55, s85, s55
	s_and_b32 s69, s4, 0x3ff

; __device__ __forceinline__ unsigned cvt_pk_bf16(float lo, float hi) { unsigned r; asm volatile("v_cvt_pk_bf16_f32 %0, %1, %2" : "=v"(r) : "v"(lo), "v"(hi)); return r; }
; #define GAS __attribute__((address_space(1)))
; #define LAS __attribute__((address_space(3)))
; __device__ __forceinline__ void conv_load(const ConvSrc& c, int lane, f32x4 (&ra)[8], f32x4 (&rb)[8]) {
;     const int nblk = c.N >> 6, kb = c.kfast ? (c.item & 31) : c.item / nblk, nb = c.kfast ? (c.item >> 5) : c.item - kb * nblk, k0 = kb * 64, n0 = nb * 64;
;     const int n4 = (lane & 15) * 4, kq = lane >> 4;
; #pragma unroll
;     for (int i = 0; i < 8; ++i) { const int kp2 = 4 * i + kq; const float* p = c.W + (size_t)(k0 + 2 * kp2) * c.N + n0 + n4; ra[i] = __builtin_nontemporal_load((const GAS f32x4*)p); rb[i] = __builtin_nontemporal_load((const GAS f32x4*)(p + c.N)); }
; }
; __device__ __forceinline__ void conv_emit(const ConvSrc& c, int lane, LAS unsigned* P, const f32x4 (&ra)[8], const f32x4 (&rb)[8]) {
;     const int nblk = c.N >> 6, kb = c.kfast ? (c.item & 31) : c.item / nblk, nb = c.kfast ? (c.item >> 5) : c.item - kb * nblk, k0 = kb * 64, n0 = nb * 64;
;     const int n4 = (lane & 15) * 4, kq = lane >> 4;
; #pragma unroll
;     for (int i = 0; i < 8; ++i) { const int kp2 = 4 * i + kq; LAS unsigned* d = P + kp2 * 65 + n4;
;         d[0] = pg8::cvt_pk_bf16(ra[i].x, rb[i].x); d[1] = pg8::cvt_pk_bf16(ra[i].y, rb[i].y); d[2] = pg8::cvt_pk_bf16(ra[i].z, rb[i].z); d[3] = pg8::cvt_pk_bf16(ra[i].w, rb[i].w); }
.LBB0_2247:
	s_lshr_b32 s4, s28, 6
	v_cvt_f32_u32_e32 v0, s4
	s_sub_i32 s47, 0, s4
	s_abs_i32 s46, s18
	s_ashr_i32 s43, s18, 31
	v_rcp_iflag_f32_e32 v0, v0
	v_mov_b32_e32 v131, v129
	v_mul_f32_e32 v0, 0x4f7ffffe, v0
	v_cvt_u32_f32_e32 v0, v0
	s_nop 0
	v_readfirstlane_b32 s48, v0
	s_mul_i32 s47, s47, s48
	s_mul_hi_u32 s47, s48, s47
	s_add_i32 s48, s48, s47
	s_mul_hi_u32 s47, s46, s48
	s_mul_i32 s48, s47, s4
	s_sub_i32 s46, s46, s48
	s_add_i32 s49, s47, 1
	s_sub_i32 s48, s46, s4
	s_cmp_ge_u32 s46, s4
	s_cselect_b32 s47, s49, s47
	s_cselect_b32 s46, s48, s46
	s_add_i32 s48, s47, 1
	s_cmp_ge_u32 s46, s4
	s_cselect_b32 s46, s48, s47
	s_xor_b32 s46, s46, s43
	s_sub_i32 s43, s46, s43
	v_lshl_add_u32 v50, s43, 6, v133
	s_mul_i32 s4, s43, s4
	v_mad_u64_u32 v[0:1], s[46:47], v50, s28, 0
	s_sub_i32 s4, s18, s4
	v_ashrrev_i32_e32 v3, 31, v50
	v_mov_b32_e32 v2, v1
	s_lshl_b32 s46, s4, 6
	v_mad_u64_u32 v[2:3], s[48:49], v3, s28, v[2:3]
	s_ashr_i32 s47, s46, 31
	v_mov_b32_e32 v1, v2
	s_waitcnt lgkmcnt(0)
	v_lshl_add_u64 v[0:1], v[0:1], 2, s[44:45]
	s_lshl_b64 s[46:47], s[46:47], 2
	v_lshl_add_u64 v[0:1], v[0:1], 0, s[46:47]
	v_lshl_add_u64 v[0:1], v[0:1], 0, v[128:129]
	s_lshl_b64 s[48:49], s[28:29], 2
	v_lshl_add_u64 v[4:5], v[0:1], 0, s[48:49]
	global_load_dwordx4 v[0:3], v[0:1], off nt
	s_nop 0
	global_load_dwordx4 v[24:27], v[4:5], off nt
	v_add_u32_e32 v4, 8, v50
	v_ashrrev_i32_e32 v7, 31, v4
	v_mad_u64_u32 v[4:5], s[54:55], v4, s28, 0
	v_mov_b32_e32 v6, v5
	v_mad_u64_u32 v[6:7], s[54:55], v7, s28, v[6:7]
	v_mov_b32_e32 v5, v6
	v_lshl_add_u64 v[4:5], v[4:5], 2, s[44:45]
	v_lshl_add_u64 v[4:5], v[4:5], 0, s[46:47]
	v_lshl_add_u64 v[4:5], v[4:5], 0, v[128:129]
	v_lshl_add_u64 v[8:9], v[4:5], 0, s[48:49]
	global_load_dwordx4 v[4:7], v[4:5], off nt
	s_nop 0
	global_load_dwordx4 v[32:35], v[8:9], off nt
	v_add_u32_e32 v8, 16, v50
	v_ashrrev_i32_e32 v11, 31, v8
	v_mad_u64_u32 v[8:9], s[54:55], v8, s28, 0
	v_mov_b32_e32 v10, v9
	v_mad_u64_u32 v[10:11], s[54:55], v11, s28, v[10:11]
	v_mov_b32_e32 v9, v10
	v_lshl_add_u64 v[8:9], v[8:9], 2, s[44:45]
	v_lshl_add_u64 v[8:9], v[8:9], 0, s[46:47]
	v_lshl_add_u64 v[8:9], v[8:9], 0, v[128:129]
	v_lshl_add_u64 v[12:13], v[8:9], 0, s[48:49]
	global_load_dwordx4 v[8:11], v[8:9], off nt
	s_nop 0
	global_load_dwordx4 v[28:31], v[12:13], off nt
	v_add_u32_e32 v12, 24, v50
	v_ashrrev_i32_e32 v15, 31, v12
	v_mad_u64_u32 v[12:13], s[54:55], v12, s28, 0
	v_mov_b32_e32 v14, v13
	v_mad_u64_u32 v[14:15], s[54:55], v15, s28, v[14:15]
	v_mov_b32_e32 v13, v14
	v_lshl_add_u64 v[12:13], v[12:13], 2, s[44:45]
	v_lshl_add_u64 v[12:13], v[12:13], 0, s[46:47]
	v_lshl_add_u64 v[12:13], v[12:13], 0, v[128:129]
	v_lshl_add_u64 v[16:17], v[12:13], 0, s[48:49]
	global_load_dwordx4 v[12:15], v[12:13], off nt
	s_nop 0
	global_load_dwordx4 v[40:43], v[16:17], off nt
	v_add_u32_e32 v16, 32, v50
	v_ashrrev_i32_e32 v19, 31, v16
	v_mad_u64_u32 v[16:17], s[54:55], v16, s28, 0
	v_mov_b32_e32 v18, v17
	v_mad_u64_u32 v[18:19], s[54:55], v19, s28, v[18:19]
	v_mov_b32_e32 v17, v18
	v_lshl_add_u64 v[16:17], v[16:17], 2, s[44:45]
	v_lshl_add_u64 v[16:17], v[16:17], 0, s[46:47]
	v_lshl_add_u64 v[16:17], v[16:17], 0, v[128:129]
	v_lshl_add_u64 v[20:21], v[16:17], 0, s[48:49]
	global_load_dwordx4 v[16:19], v[16:17], off nt
	s_nop 0
	global_load_dwordx4 v[36:39], v[20:21], off nt
	v_add_u32_e32 v20, 40, v50
	v_ashrrev_i32_e32 v23, 31, v20
	v_mad_u64_u32 v[20:21], s[54:55], v20, s28, 0
	v_mov_b32_e32 v22, v21
	v_mad_u64_u32 v[22:23], s[54:55], v23, s28, v[22:23]
	v_mov_b32_e32 v21, v22
	v_lshl_add_u64 v[20:21], v[20:21], 2, s[44:45]
	v_lshl_add_u64 v[20:21], v[20:21], 0, s[46:47]
	v_lshl_add_u64 v[20:21], v[20:21], 0, v[128:129]
	v_lshl_add_u64 v[44:45], v[20:21], 0, s[48:49]
	global_load_dwordx4 v[20:23], v[20:21], off nt
	s_nop 0
	global_load_dwordx4 v[60:63], v[44:45], off nt
	v_add_u32_e32 v44, 48, v50
	v_ashrrev_i32_e32 v47, 31, v44
	v_mad_u64_u32 v[44:45], s[54:55], v44, s28, 0
	v_mov_b32_e32 v46, v45
	v_mad_u64_u32 v[46:47], s[54:55], v47, s28, v[46:47]
	v_mov_b32_e32 v45, v46
	v_lshl_add_u64 v[44:45], v[44:45], 2, s[44:45]
	v_lshl_add_u64 v[44:45], v[44:45], 0, s[46:47]
	v_lshl_add_u64 v[44:45], v[44:45], 0, v[128:129]
	v_lshl_add_u64 v[48:49], v[44:45], 0, s[48:49]
	global_load_dwordx4 v[44:47], v[44:45], off nt
	s_nop 0
	global_load_dwordx4 v[56:59], v[48:49], off nt
	v_add_u32_e32 v48, 56, v50
	v_ashrrev_i32_e32 v51, 31, v48
	v_mad_u64_u32 v[48:49], s[54:55], v48, s28, 0
	v_mov_b32_e32 v50, v49
	v_mad_u64_u32 v[50:51], s[54:55], v51, s28, v[50:51]
	v_mov_b32_e32 v49, v50
	v_lshl_add_u64 v[48:49], v[48:49], 2, s[44:45]
	v_lshl_add_u64 v[48:49], v[48:49], 0, s[46:47]
	v_lshl_add_u64 v[48:49], v[48:49], 0, v[128:129]
	v_lshl_add_u64 v[50:51], v[48:49], 0, s[48:49]
	global_load_dwordx4 v[52:55], v[48:49], off nt
	s_nop 0
	global_load_dwordx4 v[48:51], v[50:51], off nt
	s_waitcnt vmcnt(38)
	v_cvt_pk_bf16_f32 v64, v64, v92
	ds_write_b32 v142, v64
	v_cvt_pk_bf16_f32 v64, v65, v93
	ds_write_b32 v142, v64 offset:4
	v_cvt_pk_bf16_f32 v64, v66, v94
	ds_write_b32 v142, v64 offset:8
	v_cvt_pk_bf16_f32 v64, v67, v95
	ds_write_b32 v142, v64 offset:12
	s_waitcnt vmcnt(36)
	v_cvt_pk_bf16_f32 v64, v68, v96
	ds_write_b32 v142, v64 offset:1040
	v_cvt_pk_bf16_f32 v64, v69, v97
	ds_write_b32 v142, v64 offset:1044
	v_cvt_pk_bf16_f32 v64, v70, v98
	ds_write_b32 v142, v64 offset:1048
	v_cvt_pk_bf16_f32 v64, v71, v99
	ds_write_b32 v142, v64 offset:1052
	s_waitcnt vmcnt(34)
; #define GAS __attribute__((address_space(1)))
; #define LAS __attribute__((address_space(3)))
; #define LDS_WAIT() asm volatile("s_waitcnt lgkmcnt(0)" ::: "memory")
; __device__ __forceinline__ void conv_emit(const ConvSrc& c, int lane, LAS unsigned* P, const f32x4 (&ra)[8], const f32x4 (&rb)[8]) {
;     ...
;     LDS_WAIT(); asm volatile("" ::: "memory");
;     const int cc = lane & 7;
; #pragma unroll
;     for (int jj = 0; jj < 8; ++jj) { const int n = (lane >> 3) + 8 * jj; const LAS unsigned* sp = P + (4 * cc) * 65 + n;
;         v4u o; o.x = sp[0]; o.y = sp[65]; o.z = sp[130]; o.w = sp[195];
;         bf16* dst = c.tiled ? c.WT + (size_t)((nb >> 2) * c.tiled + c.ktoff + kb) * 16384 + ((nb & 3) * 64 + n) * 64 + 8 * cc : c.WT + (size_t)(n0 + n) * c.ldk + k0 + 8 * cc;
;         __builtin_nontemporal_store(o, (GAS v4u*)dst); }
;     LDS_WAIT(); asm volatile("" ::: "memory");
	v_cvt_pk_bf16_f32 v64, v72, v100
	ds_write_b32 v142, v64 offset:2080
	v_cvt_pk_bf16_f32 v64, v73, v101
	ds_write_b32 v142, v64 offset:2084
	v_cvt_pk_bf16_f32 v64, v74, v102
	ds_write_b32 v142, v64 offset:2088
	v_cvt_pk_bf16_f32 v64, v75, v103
	ds_write_b32 v142, v64 offset:2092
	s_waitcnt vmcnt(32)
	v_cvt_pk_bf16_f32 v64, v76, v104
	ds_write_b32 v142, v64 offset:3120
	v_cvt_pk_bf16_f32 v64, v77, v105
	ds_write_b32 v142, v64 offset:3124
	v_cvt_pk_bf16_f32 v64, v78, v106
	ds_write_b32 v142, v64 offset:3128
	v_cvt_pk_bf16_f32 v64, v79, v107
	ds_write_b32 v142, v64 offset:3132
	s_waitcnt vmcnt(30)
	v_cvt_pk_bf16_f32 v64, v80, v108
	ds_write_b32 v142, v64 offset:4160
	v_cvt_pk_bf16_f32 v64, v81, v109
	ds_write_b32 v142, v64 offset:4164
	v_cvt_pk_bf16_f32 v64, v82, v110
	ds_write_b32 v142, v64 offset:4168
	v_cvt_pk_bf16_f32 v64, v83, v111
	ds_write_b32 v142, v64 offset:4172
	s_waitcnt vmcnt(28)
	v_cvt_pk_bf16_f32 v64, v84, v112
	ds_write_b32 v142, v64 offset:5200
	v_cvt_pk_bf16_f32 v64, v85, v113
	ds_write_b32 v142, v64 offset:5204
	v_cvt_pk_bf16_f32 v64, v86, v114
	ds_write_b32 v142, v64 offset:5208
	v_cvt_pk_bf16_f32 v64, v87, v115
	ds_write_b32 v142, v64 offset:5212
	s_waitcnt vmcnt(26)
	v_cvt_pk_bf16_f32 v64, v88, v116
	ds_write_b32 v142, v64 offset:6240
	v_cvt_pk_bf16_f32 v64, v89, v117
	ds_write_b32 v142, v64 offset:6244
	v_cvt_pk_bf16_f32 v64, v90, v118
	ds_write_b32 v142, v64 offset:6248
	v_cvt_pk_bf16_f32 v64, v91, v119
	ds_write_b32 v142, v64 offset:6252
	s_waitcnt vmcnt(24)
	v_cvt_pk_bf16_f32 v64, v120, v124
	ds_write_b32 v142, v64 offset:7280
	v_cvt_pk_bf16_f32 v64, v121, v125
	ds_write_b32 v142, v64 offset:7284
	v_cvt_pk_bf16_f32 v64, v122, v126
	ds_write_b32 v142, v64 offset:7288
	v_cvt_pk_bf16_f32 v64, v123, v127
	ds_write_b32 v142, v64 offset:7292
	s_ashr_i32 s4, s53, 2
	s_waitcnt lgkmcnt(0)
	s_mul_i32 s4, s4, s20
	s_add_i32 s5, s21, s5
	s_add_i32 s4, s5, s4
	ds_read2_b32 v[72:73], v134 offset1:8
	ds_read2_b32 v[64:65], v134 offset0:65 offset1:73
	ds_read2_b32 v[74:75], v134 offset0:130 offset1:138
	ds_read2_b32 v[66:67], v134 offset0:195 offset1:203
	s_ashr_i32 s5, s4, 31
	s_and_b32 s42, s42, 0xc0
	s_lshl_b64 s[4:5], s[4:5], 15
	s_add_u32 s40, s40, s4
	v_add_lshl_u32 v76, s42, v132, 6
	s_addc_u32 s41, s41, s5
	v_ashrrev_i32_e32 v77, 31, v76
	v_lshl_add_u64 v[76:77], v[76:77], 1, s[40:41]
	s_waitcnt lgkmcnt(3)
	v_mov_b32_e32 v68, v72
	s_waitcnt lgkmcnt(2)
	v_mov_b32_e32 v69, v64
	s_waitcnt lgkmcnt(1)
	v_mov_b32_e32 v70, v74
	s_waitcnt lgkmcnt(0)
	v_mov_b32_e32 v71, v66
	v_lshl_add_u64 v[76:77], v[76:77], 0, v[130:131]
	global_store_dwordx4 v[76:77], v[68:71], off
	v_mov_b32_e32 v64, v73
	v_mov_b32_e32 v66, v75
	v_add_lshl_u32 v68, s42, v135, 6
	v_ashrrev_i32_e32 v69, 31, v68
	v_lshl_add_u64 v[68:69], v[68:69], 1, s[40:41]
	v_lshl_add_u64 v[72:73], v[68:69], 0, v[130:131]
	ds_read2_b32 v[74:75], v134 offset0:16 offset1:24
	ds_read2_b32 v[68:69], v134 offset0:81 offset1:89
	ds_read2_b32 v[76:77], v134 offset0:146 offset1:154
	ds_read2_b32 v[70:71], v134 offset0:211 offset1:219
	global_store_dwordx4 v[72:73], v[64:67], off
	v_add_lshl_u32 v72, s42, v136, 6
	v_ashrrev_i32_e32 v73, 31, v72
	v_lshl_add_u64 v[72:73], v[72:73], 1, s[40:41]
	s_waitcnt lgkmcnt(3)
	v_mov_b32_e32 v64, v74
	s_waitcnt lgkmcnt(2)
	v_mov_b32_e32 v65, v68
	s_waitcnt lgkmcnt(1)
	v_mov_b32_e32 v66, v76
	s_waitcnt lgkmcnt(0)
	v_mov_b32_e32 v67, v70
	v_lshl_add_u64 v[72:73], v[72:73], 0, v[130:131]
	global_store_dwordx4 v[72:73], v[64:67], off
	v_mov_b32_e32 v68, v75
	v_mov_b32_e32 v70, v77
	v_add_lshl_u32 v64, s42, v137, 6
	v_ashrrev_i32_e32 v65, 31, v64
	v_lshl_add_u64 v[64:65], v[64:65], 1, s[40:41]
	v_lshl_add_u64 v[72:73], v[64:65], 0, v[130:131]
	ds_read2_b32 v[74:75], v134 offset0:32 offset1:40
	ds_read2_b32 v[64:65], v134 offset0:97 offset1:105
	ds_read2_b32 v[76:77], v134 offset0:162 offset1:170
	ds_read2_b32 v[66:67], v134 offset0:227 offset1:235
	global_store_dwordx4 v[72:73], v[68:71], off
	v_add_lshl_u32 v72, s42, v138, 6
	v_ashrrev_i32_e32 v73, 31, v72
	v_lshl_add_u64 v[72:73], v[72:73], 1, s[40:41]
	s_waitcnt lgkmcnt(3)
	v_mov_b32_e32 v68, v74
	s_waitcnt lgkmcnt(2)
	v_mov_b32_e32 v69, v64
	s_waitcnt lgkmcnt(1)
	v_mov_b32_e32 v70, v76
	s_waitcnt lgkmcnt(0)
	v_mov_b32_e32 v71, v66
	v_lshl_add_u64 v[72:73], v[72:73], 0, v[130:131]
	global_store_dwordx4 v[72:73], v[68:71], off
	v_mov_b32_e32 v64, v75
	v_mov_b32_e32 v66, v77
	v_add_lshl_u32 v68, s42, v139, 6
	v_ashrrev_i32_e32 v69, 31, v68
	v_lshl_add_u64 v[68:69], v[68:69], 1, s[40:41]
	v_lshl_add_u64 v[72:73], v[68:69], 0, v[130:131]
	ds_read2_b32 v[74:75], v134 offset0:48 offset1:56
	ds_read2_b32 v[68:69], v134 offset0:113 offset1:121
	ds_read2_b32 v[76:77], v134 offset0:178 offset1:186
	ds_read2_b32 v[70:71], v134 offset0:243 offset1:251
	global_store_dwordx4 v[72:73], v[64:67], off
	v_add_lshl_u32 v72, s42, v140, 6
	v_ashrrev_i32_e32 v73, 31, v72
	v_lshl_add_u64 v[72:73], v[72:73], 1, s[40:41]
	s_waitcnt lgkmcnt(3)
	v_mov_b32_e32 v64, v74
	s_waitcnt lgkmcnt(2)
	v_mov_b32_e32 v65, v68
	s_waitcnt lgkmcnt(1)
	v_mov_b32_e32 v66, v76
	s_waitcnt lgkmcnt(0)
	v_mov_b32_e32 v67, v70
	v_lshl_add_u64 v[72:73], v[72:73], 0, v[130:131]
	global_store_dwordx4 v[72:73], v[64:67], off
	v_mov_b32_e32 v68, v75
	v_mov_b32_e32 v70, v77
	v_add_lshl_u32 v64, s42, v141, 6
	v_ashrrev_i32_e32 v65, 31, v64
	v_lshl_add_u64 v[64:65], v[64:65], 1, s[40:41]
	v_lshl_add_u64 v[64:65], v[64:65], 0, v[130:131]
	global_store_dwordx4 v[64:65], v[68:71], off
	s_waitcnt lgkmcnt(0)
	s_cmp_lt_i32 s22, s17
	s_mov_b32 s4, s28
	s_cbranch_scc0 .LBB0_2288

; #define GAS __attribute__((address_space(1)))
; __device__ __forceinline__ void conv_load(const ConvSrc& c, int lane, f32x4 (&ra)[8], f32x4 (&rb)[8]) {
;     const int nblk = c.N >> 6, kb = c.kfast ? (c.item & 31) : c.item / nblk, nb = c.kfast ? (c.item >> 5) : c.item - kb * nblk, k0 = kb * 64, n0 = nb * 64;
;     const int n4 = (lane & 15) * 4, kq = lane >> 4;
; #pragma unroll
;     for (int i = 0; i < 8; ++i) { const int kp2 = 4 * i + kq; const float* p = c.W + (size_t)(k0 + 2 * kp2) * c.N + n0 + n4; ra[i] = __builtin_nontemporal_load((const GAS f32x4*)p); rb[i] = __builtin_nontemporal_load((const GAS f32x4*)(p + c.N)); }
; }
.LBB0_2267:
	s_lshr_b32 s42, s28, 6
	v_cvt_f32_u32_e32 v64, s42
	s_sub_i32 s47, 0, s42
	s_abs_i32 s43, s46
	s_ashr_i32 s21, s46, 31
	v_rcp_iflag_f32_e32 v64, v64
	s_nop 0
	v_mul_f32_e32 v64, 0x4f7ffffe, v64
	v_cvt_u32_f32_e32 v64, v64
	s_nop 0
	v_readfirstlane_b32 s48, v64
	s_mul_i32 s47, s47, s48
	s_mul_hi_u32 s47, s48, s47
	s_add_i32 s48, s48, s47
	s_mul_hi_u32 s47, s43, s48
	s_mul_i32 s48, s47, s42
	s_sub_i32 s43, s43, s48
	s_add_i32 s49, s47, 1
	s_sub_i32 s48, s43, s42
	s_cmp_ge_u32 s43, s42
	s_cselect_b32 s47, s49, s47
	s_cselect_b32 s43, s48, s43
	s_add_i32 s48, s47, 1
	s_cmp_ge_u32 s43, s42
	s_cselect_b32 s43, s48, s47
	s_xor_b32 s43, s43, s21
	s_sub_i32 s21, s43, s21
	s_mul_i32 s42, s21, s42
	v_lshl_add_u32 v120, s21, 6, v133
	s_sub_i32 s53, s46, s42
	v_mad_u64_u32 v[64:65], s[42:43], v120, s28, 0
	v_ashrrev_i32_e32 v67, 31, v120
	v_mov_b32_e32 v66, v65
	s_lshl_b32 s42, s53, 6
	v_mad_u64_u32 v[66:67], s[46:47], v67, s28, v[66:67]
	s_ashr_i32 s43, s42, 31
	v_mov_b32_e32 v65, v66
	s_waitcnt lgkmcnt(0)
	v_lshl_add_u64 v[64:65], v[64:65], 2, s[44:45]
	s_lshl_b64 s[46:47], s[42:43], 2
	v_lshl_add_u64 v[64:65], v[64:65], 0, s[46:47]
	v_lshl_add_u64 v[64:65], v[64:65], 0, v[128:129]
	s_lshl_b64 s[48:49], s[28:29], 2
	v_lshl_add_u64 v[68:69], v[64:65], 0, s[48:49]
	global_load_dwordx4 v[64:67], v[64:65], off nt
	s_nop 0
	global_load_dwordx4 v[92:95], v[68:69], off nt
	v_add_u32_e32 v68, 8, v120
	v_ashrrev_i32_e32 v71, 31, v68
	v_mad_u64_u32 v[68:69], s[54:55], v68, s28, 0
	v_mov_b32_e32 v70, v69
	v_mad_u64_u32 v[70:71], s[54:55], v71, s28, v[70:71]
	v_mov_b32_e32 v69, v70
	v_lshl_add_u64 v[68:69], v[68:69], 2, s[44:45]
	v_lshl_add_u64 v[68:69], v[68:69], 0, s[46:47]
	v_lshl_add_u64 v[68:69], v[68:69], 0, v[128:129]
	v_lshl_add_u64 v[72:73], v[68:69], 0, s[48:49]
	global_load_dwordx4 v[68:71], v[68:69], off nt
	s_nop 0
	global_load_dwordx4 v[96:99], v[72:73], off nt
	v_add_u32_e32 v72, 16, v120
	v_ashrrev_i32_e32 v75, 31, v72
	v_mad_u64_u32 v[72:73], s[54:55], v72, s28, 0
	v_mov_b32_e32 v74, v73
	v_mad_u64_u32 v[74:75], s[54:55], v75, s28, v[74:75]
	v_mov_b32_e32 v73, v74
	v_lshl_add_u64 v[72:73], v[72:73], 2, s[44:45]
	v_lshl_add_u64 v[72:73], v[72:73], 0, s[46:47]
	v_lshl_add_u64 v[72:73], v[72:73], 0, v[128:129]
	v_lshl_add_u64 v[76:77], v[72:73], 0, s[48:49]
	global_load_dwordx4 v[72:75], v[72:73], off nt
	s_nop 0
	global_load_dwordx4 v[100:103], v[76:77], off nt
	v_add_u32_e32 v76, 24, v120
	v_ashrrev_i32_e32 v79, 31, v76
	v_mad_u64_u32 v[76:77], s[54:55], v76, s28, 0
	v_mov_b32_e32 v78, v77
	v_mad_u64_u32 v[78:79], s[54:55], v79, s28, v[78:79]
	v_mov_b32_e32 v77, v78
	v_lshl_add_u64 v[76:77], v[76:77], 2, s[44:45]
	v_lshl_add_u64 v[76:77], v[76:77], 0, s[46:47]
	v_lshl_add_u64 v[76:77], v[76:77], 0, v[128:129]
	v_lshl_add_u64 v[80:81], v[76:77], 0, s[48:49]
	global_load_dwordx4 v[76:79], v[76:77], off nt
	s_nop 0
	global_load_dwordx4 v[104:107], v[80:81], off nt
	v_add_u32_e32 v80, 32, v120
	v_ashrrev_i32_e32 v83, 31, v80
	v_mad_u64_u32 v[80:81], s[54:55], v80, s28, 0
	v_mov_b32_e32 v82, v81
	v_mad_u64_u32 v[82:83], s[54:55], v83, s28, v[82:83]
	v_mov_b32_e32 v81, v82
	v_lshl_add_u64 v[80:81], v[80:81], 2, s[44:45]
	v_lshl_add_u64 v[80:81], v[80:81], 0, s[46:47]
	v_lshl_add_u64 v[80:81], v[80:81], 0, v[128:129]
	v_lshl_add_u64 v[84:85], v[80:81], 0, s[48:49]
	global_load_dwordx4 v[80:83], v[80:81], off nt
	s_nop 0
	global_load_dwordx4 v[108:111], v[84:85], off nt
	v_add_u32_e32 v84, 40, v120
	v_ashrrev_i32_e32 v87, 31, v84
	v_mad_u64_u32 v[84:85], s[54:55], v84, s28, 0
	v_mov_b32_e32 v86, v85
	v_mad_u64_u32 v[86:87], s[54:55], v87, s28, v[86:87]
	v_mov_b32_e32 v85, v86
	v_lshl_add_u64 v[84:85], v[84:85], 2, s[44:45]
	v_lshl_add_u64 v[84:85], v[84:85], 0, s[46:47]
	v_lshl_add_u64 v[84:85], v[84:85], 0, v[128:129]
	v_lshl_add_u64 v[88:89], v[84:85], 0, s[48:49]
	global_load_dwordx4 v[84:87], v[84:85], off nt
	s_nop 0
	global_load_dwordx4 v[112:115], v[88:89], off nt
	v_add_u32_e32 v88, 48, v120
	v_add_u32_e32 v120, 56, v120
	v_ashrrev_i32_e32 v91, 31, v88
	v_mad_u64_u32 v[88:89], s[54:55], v88, s28, 0
	v_ashrrev_i32_e32 v123, 31, v120
	v_mad_u64_u32 v[120:121], s[54:55], v120, s28, 0
	v_mov_b32_e32 v90, v89
	v_mov_b32_e32 v122, v121
	v_mad_u64_u32 v[90:91], s[54:55], v91, s28, v[90:91]
	v_mad_u64_u32 v[122:123], s[54:55], v123, s28, v[122:123]
	v_mov_b32_e32 v89, v90
	v_mov_b32_e32 v121, v122
	s_lshr_b32 s4, s4, 6
	v_lshl_add_u64 v[88:89], v[88:89], 2, s[44:45]
	v_cvt_f32_u32_e32 v122, s4
	v_lshl_add_u64 v[120:121], v[120:121], 2, s[44:45]
	v_lshl_add_u64 v[88:89], v[88:89], 0, s[46:47]
	v_lshl_add_u64 v[120:121], v[120:121], 0, s[46:47]
	v_lshl_add_u64 v[88:89], v[88:89], 0, v[128:129]
	v_lshl_add_u64 v[120:121], v[120:121], 0, v[128:129]
	v_lshl_add_u64 v[116:117], v[88:89], 0, s[48:49]
	v_lshl_add_u64 v[124:125], v[120:121], 0, s[48:49]
	global_load_dwordx4 v[88:91], v[88:89], off nt
	s_nop 0
	global_load_dwordx4 v[116:119], v[116:117], off nt
	v_rcp_iflag_f32_e32 v131, v122
	global_load_dwordx4 v[120:123], v[120:121], off nt
	s_nop 0
	global_load_dwordx4 v[124:127], v[124:125], off nt
	s_waitcnt vmcnt(16)
; #define GAS __attribute__((address_space(1)))
; #define LAS __attribute__((address_space(3)))
; __device__ __forceinline__ ConvSrc conv_decode(KP kp, unsigned char* ws, int it) {
;     constexpr int I_IN = 32 * 256, I_SQ = 32 * 32, I_UP = 32 * 64, I_DN = 32 * 32;
;     ConvSrc c; int r = it; c.ldk = 2048; c.kfast = 0; c.tiled = 32; c.ktoff = 0;
;     if (r < I_IN) { c.W = (const float*)KIN(6); c.WT = (bf16*)(ws + WS_WIN); c.N = 16384; c.item = r; return c; } r -= I_IN;
;     if (r < I_SQ) { c.W = (const float*)KIN(13); c.WT = (bf16*)(ws + WS_WAO); c.N = 2048; c.item = r; c.ldk = 4096; c.tiled = 64; return c; } r -= I_SQ;
;     if (r < I_SQ) { c.W = (const float*)KIN(14); c.WT = (bf16*)(ws + WS_WAO); c.N = 2048; c.item = r; c.ldk = 4096; c.tiled = 64; c.ktoff = 32; return c; } r -= I_SQ;
;     if (r < I_SQ) { c.W = (const float*)KIN(15); c.WT = (bf16*)(ws + WS_WO); c.N = 2048; c.item = r; return c; } r -= I_SQ;
;     if (r < NE * I_UP) { const int e = r / I_UP; c.W = (const float*)KIN(19) + (size_t)e * 2048 * 4096; c.WT = (bf16*)(ws + WS_WUP) + (size_t)e * 4096 * 2048; c.N = 4096; c.item = r - e * I_UP; return c; } r -= NE * I_UP;
; __device__ __forceinline__ void conv_emit(const ConvSrc& c, int lane, LAS unsigned* P, const f32x4 (&ra)[8], const f32x4 (&rb)[8]) {
;     const int nblk = c.N >> 6, kb = c.kfast ? (c.item & 31) : c.item / nblk, nb = c.kfast ? (c.item >> 5) : c.item - kb * nblk, k0 = kb * 64, n0 = nb * 64;
;     const int n4 = (lane & 15) * 4, kq = lane >> 4;
; #pragma unroll
;     for (int i = 0; i < 8; ++i) { const int kp2 = 4 * i + kq; LAS unsigned* d = P + kp2 * 65 + n4;
;         d[0] = pg8::cvt_pk_bf16(ra[i].x, rb[i].x); d[1] = pg8::cvt_pk_bf16(ra[i].y, rb[i].y); d[2] = pg8::cvt_pk_bf16(ra[i].z, rb[i].z); d[3] = pg8::cvt_pk_bf16(ra[i].w, rb[i].w); }
;     LDS_WAIT(); asm volatile("" ::: "memory");
;     const int cc = lane & 7;
; #pragma unroll
;     for (int jj = 0; jj < 8; ++jj) { const int n = (lane >> 3) + 8 * jj; const LAS unsigned* sp = P + (4 * cc) * 65 + n;
;         v4u o; o.x = sp[0]; o.y = sp[65]; o.z = sp[130]; o.w = sp[195];
;         bf16* dst = c.tiled ? c.WT + (size_t)((nb >> 2) * c.tiled + c.ktoff + kb) * 16384 + ((nb & 3) * 64 + n) * 64 + 8 * cc : c.WT + (size_t)(n0 + n) * c.ldk + k0 + 8 * cc;
;         __builtin_nontemporal_store(o, (GAS v4u*)dst); }
;     LDS_WAIT(); asm volatile("" ::: "memory");
	v_cvt_pk_bf16_f32 v0, v0, v24
	ds_write_b32 v142, v0
	v_cvt_pk_bf16_f32 v0, v1, v25
	ds_write_b32 v142, v0 offset:4
	v_cvt_pk_bf16_f32 v0, v2, v26
	ds_write_b32 v142, v0 offset:8
	v_cvt_pk_bf16_f32 v0, v3, v27
	ds_write_b32 v142, v0 offset:12
	v_cvt_pk_bf16_f32 v0, v4, v32
	ds_write_b32 v142, v0 offset:1040
	v_cvt_pk_bf16_f32 v0, v5, v33
	ds_write_b32 v142, v0 offset:1044
	v_cvt_pk_bf16_f32 v0, v6, v34
	ds_write_b32 v142, v0 offset:1048
	v_cvt_pk_bf16_f32 v0, v7, v35
	ds_write_b32 v142, v0 offset:1052
	v_cvt_pk_bf16_f32 v0, v8, v28
	v_mul_f32_e32 v131, 0x4f7ffffe, v131
	ds_write_b32 v142, v0 offset:2080
	v_cvt_pk_bf16_f32 v0, v9, v29
	v_cvt_u32_f32_e32 v131, v131
	ds_write_b32 v142, v0 offset:2084
	v_cvt_pk_bf16_f32 v0, v10, v30
	ds_write_b32 v142, v0 offset:2088
	v_cvt_pk_bf16_f32 v0, v11, v31
	ds_write_b32 v142, v0 offset:2092
	v_cvt_pk_bf16_f32 v0, v12, v40
	ds_write_b32 v142, v0 offset:3120
	v_cvt_pk_bf16_f32 v0, v13, v41
	s_sub_i32 s44, 0, s4
	v_readfirstlane_b32 s45, v131
	ds_write_b32 v142, v0 offset:3124
	v_cvt_pk_bf16_f32 v0, v14, v42
	s_mul_i32 s44, s44, s45
	ds_write_b32 v142, v0 offset:3128
	v_cvt_pk_bf16_f32 v0, v15, v43
	s_mul_hi_u32 s44, s45, s44
	ds_write_b32 v142, v0 offset:3132
	v_cvt_pk_bf16_f32 v0, v16, v36
	s_abs_i32 s43, s18
	s_add_i32 s45, s45, s44
	ds_write_b32 v142, v0 offset:4160
	v_cvt_pk_bf16_f32 v0, v17, v37
	s_mul_hi_u32 s44, s43, s45
	ds_write_b32 v142, v0 offset:4164
	v_cvt_pk_bf16_f32 v0, v18, v38
	s_mul_i32 s45, s44, s4
	ds_write_b32 v142, v0 offset:4168
	v_cvt_pk_bf16_f32 v0, v19, v39
	s_sub_i32 s43, s43, s45
	ds_write_b32 v142, v0 offset:4172
	v_cvt_pk_bf16_f32 v0, v20, v60
	s_ashr_i32 s28, s18, 31
	s_add_i32 s45, s44, 1
	s_sub_i32 s46, s43, s4
	ds_write_b32 v142, v0 offset:5200
	v_cvt_pk_bf16_f32 v0, v21, v61
	s_cmp_ge_u32 s43, s4
	ds_write_b32 v142, v0 offset:5204
	v_cvt_pk_bf16_f32 v0, v22, v62
	s_cselect_b32 s44, s45, s44
	ds_write_b32 v142, v0 offset:5208
	v_cvt_pk_bf16_f32 v0, v23, v63
	s_cselect_b32 s43, s46, s43
	s_add_i32 s45, s44, 1
	ds_write_b32 v142, v0 offset:5212
	v_cvt_pk_bf16_f32 v0, v44, v56
	s_cmp_ge_u32 s43, s4
	ds_write_b32 v142, v0 offset:6240
	v_cvt_pk_bf16_f32 v0, v45, v57
	s_cselect_b32 s43, s45, s44
	ds_write_b32 v142, v0 offset:6244
	v_cvt_pk_bf16_f32 v0, v46, v58
	s_xor_b32 s43, s43, s28
	ds_write_b32 v142, v0 offset:6248
	v_cvt_pk_bf16_f32 v0, v47, v59
	s_sub_i32 s28, s43, s28
	ds_write_b32 v142, v0 offset:6252
	v_cvt_pk_bf16_f32 v0, v52, v48
	s_mul_i32 s4, s28, s4
	ds_write_b32 v142, v0 offset:7280
	v_cvt_pk_bf16_f32 v0, v53, v49
	s_sub_i32 s4, s18, s4
	ds_write_b32 v142, v0 offset:7284
	v_cvt_pk_bf16_f32 v0, v54, v50
	ds_write_b32 v142, v0 offset:7288
	v_cvt_pk_bf16_f32 v0, v55, v51
	ds_write_b32 v142, v0 offset:7292
	s_lshl_b32 s18, s4, 6
	s_ashr_i32 s4, s4, 2
	s_waitcnt lgkmcnt(0)
	s_mul_i32 s4, s4, s52
	s_add_i32 s28, s28, s51
	s_add_i32 s44, s28, s4
	ds_read2_b32 v[8:9], v134 offset1:8
	ds_read2_b32 v[0:1], v134 offset0:65 offset1:73
	ds_read2_b32 v[10:11], v134 offset0:130 offset1:138
	ds_read2_b32 v[2:3], v134 offset0:195 offset1:203
	s_ashr_i32 s45, s44, 31
	s_and_b32 s18, s18, 0xc0
	s_lshl_b64 s[44:45], s[44:45], 15
	s_add_u32 s30, s30, s44
	v_add_lshl_u32 v12, s18, v132, 6
	s_addc_u32 s31, s31, s45
	v_ashrrev_i32_e32 v13, 31, v12
	v_lshl_add_u64 v[12:13], v[12:13], 1, s[30:31]
	v_mov_b32_e32 v131, v129
	s_waitcnt lgkmcnt(3)
	v_mov_b32_e32 v4, v8
	s_waitcnt lgkmcnt(2)
	v_mov_b32_e32 v5, v0
	s_waitcnt lgkmcnt(1)
	v_mov_b32_e32 v6, v10
	s_waitcnt lgkmcnt(0)
	v_mov_b32_e32 v7, v2
	v_lshl_add_u64 v[12:13], v[12:13], 0, v[130:131]
	global_store_dwordx4 v[12:13], v[4:7], off
	v_mov_b32_e32 v0, v9
	v_mov_b32_e32 v2, v11
	v_add_lshl_u32 v4, s18, v135, 6
	v_ashrrev_i32_e32 v5, 31, v4
	v_lshl_add_u64 v[4:5], v[4:5], 1, s[30:31]
	v_lshl_add_u64 v[8:9], v[4:5], 0, v[130:131]
	ds_read2_b32 v[10:11], v134 offset0:16 offset1:24
	ds_read2_b32 v[4:5], v134 offset0:81 offset1:89
	ds_read2_b32 v[12:13], v134 offset0:146 offset1:154
	ds_read2_b32 v[6:7], v134 offset0:211 offset1:219
	global_store_dwordx4 v[8:9], v[0:3], off
	v_add_lshl_u32 v8, s18, v136, 6
	v_ashrrev_i32_e32 v9, 31, v8
	v_lshl_add_u64 v[8:9], v[8:9], 1, s[30:31]
	s_waitcnt lgkmcnt(3)
	v_mov_b32_e32 v0, v10
	s_waitcnt lgkmcnt(2)
	v_mov_b32_e32 v1, v4
	s_waitcnt lgkmcnt(1)
	v_mov_b32_e32 v2, v12
	s_waitcnt lgkmcnt(0)
	v_mov_b32_e32 v3, v6
	v_lshl_add_u64 v[8:9], v[8:9], 0, v[130:131]
	global_store_dwordx4 v[8:9], v[0:3], off
	v_mov_b32_e32 v4, v11
	v_mov_b32_e32 v6, v13
	v_add_lshl_u32 v0, s18, v137, 6
	v_ashrrev_i32_e32 v1, 31, v0
	v_lshl_add_u64 v[0:1], v[0:1], 1, s[30:31]
	v_lshl_add_u64 v[8:9], v[0:1], 0, v[130:131]
	ds_read2_b32 v[10:11], v134 offset0:32 offset1:40
	ds_read2_b32 v[0:1], v134 offset0:97 offset1:105
	ds_read2_b32 v[12:13], v134 offset0:162 offset1:170
	ds_read2_b32 v[2:3], v134 offset0:227 offset1:235
	global_store_dwordx4 v[8:9], v[4:7], off
	v_add_lshl_u32 v8, s18, v138, 6
	v_ashrrev_i32_e32 v9, 31, v8
	v_lshl_add_u64 v[8:9], v[8:9], 1, s[30:31]
	s_waitcnt lgkmcnt(3)
	v_mov_b32_e32 v4, v10
	s_waitcnt lgkmcnt(2)
	v_mov_b32_e32 v5, v0
	s_waitcnt lgkmcnt(1)
	v_mov_b32_e32 v6, v12
	s_waitcnt lgkmcnt(0)
	v_mov_b32_e32 v7, v2
	v_lshl_add_u64 v[8:9], v[8:9], 0, v[130:131]
	global_store_dwordx4 v[8:9], v[4:7], off
	v_mov_b32_e32 v0, v11
	v_mov_b32_e32 v2, v13
	v_add_lshl_u32 v4, s18, v139, 6
	v_ashrrev_i32_e32 v5, 31, v4
	v_lshl_add_u64 v[4:5], v[4:5], 1, s[30:31]
	v_lshl_add_u64 v[8:9], v[4:5], 0, v[130:131]
	ds_read2_b32 v[10:11], v134 offset0:48 offset1:56
	ds_read2_b32 v[4:5], v134 offset0:113 offset1:121
	ds_read2_b32 v[12:13], v134 offset0:178 offset1:186
	ds_read2_b32 v[6:7], v134 offset0:243 offset1:251
	global_store_dwordx4 v[8:9], v[0:3], off
	v_add_lshl_u32 v8, s18, v140, 6
	v_ashrrev_i32_e32 v9, 31, v8
	v_lshl_add_u64 v[8:9], v[8:9], 1, s[30:31]
	s_waitcnt lgkmcnt(3)
	v_mov_b32_e32 v0, v10
	s_waitcnt lgkmcnt(2)
	v_mov_b32_e32 v1, v4
	s_waitcnt lgkmcnt(1)
	v_mov_b32_e32 v2, v12
	s_waitcnt lgkmcnt(0)
	v_mov_b32_e32 v3, v6
	v_lshl_add_u64 v[8:9], v[8:9], 0, v[130:131]
	global_store_dwordx4 v[8:9], v[0:3], off
	v_mov_b32_e32 v4, v11
	v_mov_b32_e32 v6, v13
	v_add_lshl_u32 v0, s18, v141, 6
	v_ashrrev_i32_e32 v1, 31, v0
	v_lshl_add_u64 v[0:1], v[0:1], 1, s[30:31]
	v_lshl_add_u64 v[0:1], v[0:1], 0, v[130:131]
	global_store_dwordx4 v[0:1], v[4:7], off
	s_waitcnt lgkmcnt(0)
	s_add_i32 s22, s22, 16
	s_min_i32 s4, s22, s23
	s_cmpk_gt_i32 s4, 0x1fff
	s_mov_b64 s[46:47], -1
	s_cbranch_scc0 .LBB0_2284
	s_cmpk_gt_u32 s4, 0x23ff
	s_cbranch_scc0 .LBB0_2281
	s_cmpk_gt_u32 s4, 0x27ff
	s_cbranch_scc0 .LBB0_2279
	s_cmpk_gt_u32 s4, 0x2bff
	s_cbranch_scc0 .LBB0_2276
	s_cmp_gt_u32 s4, 0x12bff
	s_cbranch_scc0 .LBB0_2273
	s_load_dwordx2 s[30:31], s[2:3], 0xa8
	s_add_i32 s18, s4, 0xfffed400
	s_lshr_b32 s28, s18, 10
	s_lshl_b64 s[44:45], s[28:29], 24
	s_mov_b64 s[46:47], 0
	s_waitcnt lgkmcnt(0)
	s_add_u32 s44, s30, s44
	s_addc_u32 s45, s31, s45
	s_lshl_b64 s[30:31], s[28:29], 23
	s_add_u32 s30, s19, s30
	s_addc_u32 s31, s24, s31
	s_and_b32 s18, s4, 0x3ff
